# all four GEMM instances: first K-trip peeled with SrcC=0 (no per-unit accumulator zeroing); M1 chunk-KV LDS reads pipelined 3 deep; attention tail PV blocks batch their LDS reads
# speedup vs baseline: 1.0315x; 1.0156x over previous
.LBB0_242:
	v_mov_b32_e32 v163, v0
	v_mov_b32_e32 v167, v0
	s_add_u32 s85, s20, 0x100
	s_addc_u32 s89, s21, 0
	v_lshl_add_u64 v[178:179], s[80:81], 0, v[166:167]
	v_lshl_add_u64 v[180:181], s[80:81], 0, v[162:163]
	s_mov_b32 s92, -2
	s_mov_b64 s[90:91], 0
	s_waitcnt vmcnt(0)
	v_add_u32_e32 v2, s23, v197
	v_add_u32_e32 v14, s66, v197
	s_add_u32 s8, s90, 0x100
	ds_read_b128 v[18:21], v2
	ds_read_b128 v[22:25], v2 offset:1024
	ds_read_b128 v[26:29], v2 offset:2048
	ds_read_b128 v[30:33], v2 offset:3072
	ds_read_b128 v[2:5], v14
	ds_read_b128 v[6:9], v14 offset:1024
	ds_read_b128 v[10:13], v14 offset:2048
	ds_read_b128 v[14:17], v14 offset:3072
	s_addc_u32 s9, s91, 0
	s_add_u32 s62, s85, s90
	s_addc_u32 s63, s89, s91
	s_cmpk_eq_i32 s90, 0x300
	s_cselect_b64 vcc, -1, 0
	s_and_b64 s[20:21], vcc, exec
	v_cndmask_b32_e32 v188, v164, v200, vcc
	v_cndmask_b32_e32 v186, v168, v201, vcc
	v_cndmask_b32_e32 v163, v162, v202, vcc
	v_cndmask_b32_e32 v165, v166, v203, vcc
	s_cselect_b32 s21, s87, s63
	s_cselect_b32 s20, s86, s62
	s_cselect_b32 s62, 0, s8
	v_lshl_add_u64 v[182:183], v[180:181], 0, s[90:91]
	s_add_i32 m0, s68, 0xc000
	ds_read_b128 v[218:221], v199
	ds_read_b128 v[222:225], v199 offset:1024
	ds_read_b128 v[226:229], v199 offset:2048
	ds_read_b128 v[230:233], v199 offset:3072
	ds_read_b128 v[234:237], v199 offset:4096
	ds_read_b128 v[238:241], v199 offset:5120
	ds_read_b128 v[242:245], v199 offset:6144
	ds_read_b128 v[246:249], v199 offset:7168
	global_load_lds_dwordx4 v[182:183], off
	v_lshl_add_u64 v[182:183], v[178:179], 0, s[90:91]
	s_add_i32 m0, s68, 0xe000
	s_nop 0
	global_load_lds_dwordx4 v[182:183], off
	s_waitcnt vmcnt(8)
	s_waitcnt lgkmcnt(0)
	s_barrier
	s_setprio 1
	s_waitcnt lgkmcnt(0)
	v_mfma_scale_f32_16x16x128_f8f6f4 v[158:161], v[18:25], v[218:225], 0, v193, v193 op_sel_hi:[0,0,0]
	v_mfma_scale_f32_16x16x128_f8f6f4 v[154:157], v[26:33], v[218:225], 0, v193, v193 op_sel_hi:[0,0,0]
	v_mfma_scale_f32_16x16x128_f8f6f4 v[142:145], v[18:25], v[226:233], 0, v193, v193 op_sel_hi:[0,0,0]
	v_mfma_scale_f32_16x16x128_f8f6f4 v[138:141], v[26:33], v[226:233], 0, v193, v193 op_sel_hi:[0,0,0]
	v_mfma_scale_f32_16x16x128_f8f6f4 v[126:129], v[18:25], v[234:241], 0, v193, v193 op_sel_hi:[0,0,0]
	v_mfma_scale_f32_16x16x128_f8f6f4 v[122:125], v[26:33], v[234:241], 0, v193, v193 op_sel_hi:[0,0,0]
	v_mfma_scale_f32_16x16x128_f8f6f4 v[110:113], v[18:25], v[242:249], 0, v193, v193 op_sel_hi:[0,0,0]
	v_mfma_scale_f32_16x16x128_f8f6f4 v[106:109], v[26:33], v[242:249], 0, v193, v193 op_sel_hi:[0,0,0]
	s_setprio 0
	s_setprio 1
	v_mfma_scale_f32_16x16x128_f8f6f4 v[150:153], v[2:9], v[218:225], 0, v193, v193 op_sel_hi:[0,0,0]
	v_mfma_scale_f32_16x16x128_f8f6f4 v[146:149], v[10:17], v[218:225], 0, v193, v193 op_sel_hi:[0,0,0]
	v_mfma_scale_f32_16x16x128_f8f6f4 v[134:137], v[2:9], v[226:233], 0, v193, v193 op_sel_hi:[0,0,0]
	v_mfma_scale_f32_16x16x128_f8f6f4 v[130:133], v[10:17], v[226:233], 0, v193, v193 op_sel_hi:[0,0,0]
	v_mfma_scale_f32_16x16x128_f8f6f4 v[118:121], v[2:9], v[234:241], 0, v193, v193 op_sel_hi:[0,0,0]
	v_mfma_scale_f32_16x16x128_f8f6f4 v[114:117], v[10:17], v[234:241], 0, v193, v193 op_sel_hi:[0,0,0]
	v_mfma_scale_f32_16x16x128_f8f6f4 v[102:105], v[2:9], v[242:249], 0, v193, v193 op_sel_hi:[0,0,0]
	v_mfma_scale_f32_16x16x128_f8f6f4 v[98:101], v[10:17], v[242:249], 0, v193, v193 op_sel_hi:[0,0,0]
	s_setprio 0
	s_barrier
	s_mov_b32 m0, s59
	v_lshl_add_u64 v[182:183], s[20:21], 0, v[170:171]
	s_add_u32 s90, s20, 0x20000
	ds_read_b128 v[218:221], v199 offset:16384
	ds_read_b128 v[222:225], v199 offset:17408
	ds_read_b128 v[226:229], v199 offset:18432
	ds_read_b128 v[230:233], v199 offset:19456
	ds_read_b128 v[234:237], v199 offset:20480
	ds_read_b128 v[238:241], v199 offset:21504
	ds_read_b128 v[242:245], v199 offset:22528
	ds_read_b128 v[246:249], v199 offset:23552
	global_load_lds_dwordx4 v[182:183], off
	v_lshl_add_u64 v[184:185], s[20:21], 0, v[172:173]
	s_mov_b32 m0, s65
	s_addc_u32 s91, s21, 0
	global_load_lds_dwordx4 v[184:185], off
	v_lshl_add_u64 v[204:205], s[90:91], 0, v[170:171]
	s_mov_b32 m0, s67
	v_mov_b32_e32 v189, v0
	global_load_lds_dwordx4 v[204:205], off
	v_lshl_add_u64 v[204:205], s[90:91], 0, v[172:173]
	s_mov_b32 m0, s10
	s_add_u32 s90, s12, s62
	global_load_lds_dwordx4 v[204:205], off
	s_addc_u32 s91, s13, 0
	s_mov_b32 m0, s68
	v_mov_b32_e32 v187, v0
	global_load_lds_dwordx4 v188, s[90:91]
	s_mov_b32 m0, s71
	v_lshl_add_u64 v[188:189], s[90:91], 0, v[188:189]
	global_load_lds_dwordx4 v186, s[90:91]
	s_waitcnt vmcnt(8)
	s_waitcnt lgkmcnt(0)
	v_lshl_add_u64 v[186:187], s[90:91], 0, v[186:187]
	s_barrier
	s_setprio 1
	s_waitcnt lgkmcnt(0)
	v_mfma_scale_f32_16x16x128_f8f6f4 v[94:97], v[18:25], v[218:225], 0, v193, v193 op_sel_hi:[0,0,0]
	v_mfma_scale_f32_16x16x128_f8f6f4 v[90:93], v[26:33], v[218:225], 0, v193, v193 op_sel_hi:[0,0,0]
	v_mfma_scale_f32_16x16x128_f8f6f4 v[78:81], v[18:25], v[226:233], 0, v193, v193 op_sel_hi:[0,0,0]
	v_mfma_scale_f32_16x16x128_f8f6f4 v[74:77], v[26:33], v[226:233], 0, v193, v193 op_sel_hi:[0,0,0]
	v_mfma_scale_f32_16x16x128_f8f6f4 v[54:57], v[18:25], v[234:241], 0, v193, v193 op_sel_hi:[0,0,0]
	v_mfma_scale_f32_16x16x128_f8f6f4 v[50:53], v[26:33], v[234:241], 0, v193, v193 op_sel_hi:[0,0,0]
	v_mfma_scale_f32_16x16x128_f8f6f4 v[38:41], v[18:25], v[242:249], 0, v193, v193 op_sel_hi:[0,0,0]
	v_mfma_scale_f32_16x16x128_f8f6f4 v[34:37], v[26:33], v[242:249], 0, v193, v193 op_sel_hi:[0,0,0]
	s_setprio 0
	s_setprio 1
	v_mfma_scale_f32_16x16x128_f8f6f4 v[86:89], v[2:9], v[218:225], 0, v193, v193 op_sel_hi:[0,0,0]
	v_mfma_scale_f32_16x16x128_f8f6f4 v[82:85], v[10:17], v[218:225], 0, v193, v193 op_sel_hi:[0,0,0]
	v_mfma_scale_f32_16x16x128_f8f6f4 v[70:73], v[2:9], v[226:233], 0, v193, v193 op_sel_hi:[0,0,0]
	v_mfma_scale_f32_16x16x128_f8f6f4 v[66:69], v[10:17], v[226:233], 0, v193, v193 op_sel_hi:[0,0,0]
	v_mfma_scale_f32_16x16x128_f8f6f4 v[62:65], v[2:9], v[234:241], 0, v193, v193 op_sel_hi:[0,0,0]
	v_mfma_scale_f32_16x16x128_f8f6f4 v[58:61], v[10:17], v[234:241], 0, v193, v193 op_sel_hi:[0,0,0]
	v_mfma_scale_f32_16x16x128_f8f6f4 v[46:49], v[2:9], v[242:249], 0, v193, v193 op_sel_hi:[0,0,0]
	v_mfma_scale_f32_16x16x128_f8f6f4 v[42:45], v[10:17], v[242:249], 0, v193, v193 op_sel_hi:[0,0,0]
	s_setprio 0
	s_barrier
	v_add_u32_e32 v14, s3, v197
	v_add_u32_e32 v30, s52, v197
	ds_read_b128 v[2:5], v14
	ds_read_b128 v[6:9], v14 offset:1024
	ds_read_b128 v[10:13], v14 offset:2048
	ds_read_b128 v[14:17], v14 offset:3072
	ds_read_b128 v[18:21], v30
	ds_read_b128 v[22:25], v30 offset:1024
	ds_read_b128 v[26:29], v30 offset:2048
	ds_read_b128 v[30:33], v30 offset:3072
	s_mov_b32 m0, s72
	ds_read_b128 v[218:221], v199 offset:32768
	ds_read_b128 v[222:225], v199 offset:33792
	ds_read_b128 v[226:229], v199 offset:34816
	ds_read_b128 v[230:233], v199 offset:35840
	ds_read_b128 v[234:237], v199 offset:36864
	ds_read_b128 v[238:241], v199 offset:37888
	ds_read_b128 v[242:245], v199 offset:38912
	ds_read_b128 v[246:249], v199 offset:39936
	global_load_lds_dwordx4 v163, s[90:91]
	s_mov_b32 m0, s73
	s_nop 0
	global_load_lds_dwordx4 v165, s[90:91]
	s_waitcnt vmcnt(8)
	s_waitcnt lgkmcnt(0)
	s_barrier
	s_setprio 1
	s_waitcnt lgkmcnt(0)
	v_mfma_scale_f32_16x16x128_f8f6f4 v[158:161], v[2:9], v[218:225], v[158:161], v193, v193 op_sel_hi:[0,0,0]
	v_mfma_scale_f32_16x16x128_f8f6f4 v[154:157], v[10:17], v[218:225], v[154:157], v193, v193 op_sel_hi:[0,0,0]
	v_mfma_scale_f32_16x16x128_f8f6f4 v[142:145], v[2:9], v[226:233], v[142:145], v193, v193 op_sel_hi:[0,0,0]
	v_mfma_scale_f32_16x16x128_f8f6f4 v[138:141], v[10:17], v[226:233], v[138:141], v193, v193 op_sel_hi:[0,0,0]
	v_mfma_scale_f32_16x16x128_f8f6f4 v[126:129], v[2:9], v[234:241], v[126:129], v193, v193 op_sel_hi:[0,0,0]
	v_mfma_scale_f32_16x16x128_f8f6f4 v[122:125], v[10:17], v[234:241], v[122:125], v193, v193 op_sel_hi:[0,0,0]
	v_mfma_scale_f32_16x16x128_f8f6f4 v[110:113], v[2:9], v[242:249], v[110:113], v193, v193 op_sel_hi:[0,0,0]
	v_mfma_scale_f32_16x16x128_f8f6f4 v[106:109], v[10:17], v[242:249], v[106:109], v193, v193 op_sel_hi:[0,0,0]
	s_setprio 0
	s_setprio 1
	v_mfma_scale_f32_16x16x128_f8f6f4 v[150:153], v[18:25], v[218:225], v[150:153], v193, v193 op_sel_hi:[0,0,0]
	v_mfma_scale_f32_16x16x128_f8f6f4 v[146:149], v[26:33], v[218:225], v[146:149], v193, v193 op_sel_hi:[0,0,0]
	v_mfma_scale_f32_16x16x128_f8f6f4 v[134:137], v[18:25], v[226:233], v[134:137], v193, v193 op_sel_hi:[0,0,0]
	v_mfma_scale_f32_16x16x128_f8f6f4 v[130:133], v[26:33], v[226:233], v[130:133], v193, v193 op_sel_hi:[0,0,0]
	v_mfma_scale_f32_16x16x128_f8f6f4 v[118:121], v[18:25], v[234:241], v[118:121], v193, v193 op_sel_hi:[0,0,0]
	v_mfma_scale_f32_16x16x128_f8f6f4 v[114:117], v[26:33], v[234:241], v[114:117], v193, v193 op_sel_hi:[0,0,0]
	v_mfma_scale_f32_16x16x128_f8f6f4 v[102:105], v[18:25], v[242:249], v[102:105], v193, v193 op_sel_hi:[0,0,0]
	v_mfma_scale_f32_16x16x128_f8f6f4 v[98:101], v[26:33], v[242:249], v[98:101], v193, v193 op_sel_hi:[0,0,0]
	s_setprio 0
	s_barrier
	s_mov_b32 m0, s64
	v_lshl_add_u64 v[182:183], v[182:183], 0, s[38:39]
	s_add_u32 s20, s20, 0x20080
	ds_read_b128 v[218:221], v199 offset:49152
	ds_read_b128 v[222:225], v199 offset:50176
	ds_read_b128 v[226:229], v199 offset:51200
	ds_read_b128 v[230:233], v199 offset:52224
	ds_read_b128 v[234:237], v199 offset:53248
	ds_read_b128 v[238:241], v199 offset:54272
	ds_read_b128 v[242:245], v199 offset:55296
	ds_read_b128 v[246:249], v199 offset:56320
	global_load_lds_dwordx4 v[182:183], off
	v_lshl_add_u64 v[182:183], v[184:185], 0, s[38:39]
	s_mov_b32 m0, s2
	s_addc_u32 s21, s21, 0
	global_load_lds_dwordx4 v[182:183], off
	v_lshl_add_u64 v[182:183], s[20:21], 0, v[170:171]
	s_mov_b32 m0, s69
	s_nop 0
	global_load_lds_dwordx4 v[182:183], off
	v_lshl_add_u64 v[182:183], s[20:21], 0, v[172:173]
	s_mov_b32 m0, s51
	s_nop 0
	global_load_lds_dwordx4 v[182:183], off
	v_lshl_add_u64 v[182:183], v[188:189], 0, s[38:39]
	s_mov_b32 m0, s45
	s_nop 0
	global_load_lds_dwordx4 v[182:183], off
	v_lshl_add_u64 v[182:183], v[186:187], 0, s[38:39]
	s_mov_b32 m0, s27
	s_nop 0
	global_load_lds_dwordx4 v[182:183], off
	s_waitcnt vmcnt(8)
	s_waitcnt lgkmcnt(0)
	s_barrier
	s_setprio 1
	s_waitcnt lgkmcnt(0)
	v_mfma_scale_f32_16x16x128_f8f6f4 v[94:97], v[2:9], v[218:225], v[94:97], v193, v193 op_sel_hi:[0,0,0]
	v_mfma_scale_f32_16x16x128_f8f6f4 v[90:93], v[10:17], v[218:225], v[90:93], v193, v193 op_sel_hi:[0,0,0]
	v_mfma_scale_f32_16x16x128_f8f6f4 v[78:81], v[2:9], v[226:233], v[78:81], v193, v193 op_sel_hi:[0,0,0]
	v_mfma_scale_f32_16x16x128_f8f6f4 v[74:77], v[10:17], v[226:233], v[74:77], v193, v193 op_sel_hi:[0,0,0]
	v_mfma_scale_f32_16x16x128_f8f6f4 v[54:57], v[2:9], v[234:241], v[54:57], v193, v193 op_sel_hi:[0,0,0]
	v_mfma_scale_f32_16x16x128_f8f6f4 v[50:53], v[10:17], v[234:241], v[50:53], v193, v193 op_sel_hi:[0,0,0]
	v_mfma_scale_f32_16x16x128_f8f6f4 v[38:41], v[2:9], v[242:249], v[38:41], v193, v193 op_sel_hi:[0,0,0]
	v_mfma_scale_f32_16x16x128_f8f6f4 v[34:37], v[10:17], v[242:249], v[34:37], v193, v193 op_sel_hi:[0,0,0]
	s_setprio 0
	s_setprio 1
	v_mfma_scale_f32_16x16x128_f8f6f4 v[86:89], v[18:25], v[218:225], v[86:89], v193, v193 op_sel_hi:[0,0,0]
	v_mfma_scale_f32_16x16x128_f8f6f4 v[82:85], v[26:33], v[218:225], v[82:85], v193, v193 op_sel_hi:[0,0,0]
	v_mfma_scale_f32_16x16x128_f8f6f4 v[70:73], v[18:25], v[226:233], v[70:73], v193, v193 op_sel_hi:[0,0,0]
	v_mfma_scale_f32_16x16x128_f8f6f4 v[66:69], v[26:33], v[226:233], v[66:69], v193, v193 op_sel_hi:[0,0,0]
	v_mfma_scale_f32_16x16x128_f8f6f4 v[62:65], v[18:25], v[234:241], v[62:65], v193, v193 op_sel_hi:[0,0,0]
	v_mfma_scale_f32_16x16x128_f8f6f4 v[58:61], v[26:33], v[234:241], v[58:61], v193, v193 op_sel_hi:[0,0,0]
	v_mfma_scale_f32_16x16x128_f8f6f4 v[46:49], v[18:25], v[242:249], v[46:49], v193, v193 op_sel_hi:[0,0,0]
	v_mfma_scale_f32_16x16x128_f8f6f4 v[42:45], v[26:33], v[242:249], v[42:45], v193, v193 op_sel_hi:[0,0,0]
	s_setprio 0
	s_barrier
	s_add_i32 s92, s92, 2
	s_cmp_gt_u32 s92, 5
	s_mov_b64 s[90:91], s[8:9]

.LBB0_326:
	v_mul_f32_e32 v2, 0xbfb8aa3b, v2
	v_mul_f32_e32 v1, 0xbfb8aa3b, v1
	v_mul_f32_e32 v3, v1, v58
	v_mul_f32_e32 v16, v2, v59
	v_exp_f32_e32 v3, v3
	v_exp_f32_e32 v16, v16
	s_waitcnt vmcnt(3)
	ds_write_b128 v62, v[34:37]
	s_waitcnt vmcnt(2)
	v_lshlrev_b32_e32 v17, 16, v12
	v_and_b32_e32 v34, 0xffff0000, v12
	v_mul_f32_e32 v12, v3, v17
	v_mul_f32_e32 v35, v3, v34
	v_mul_f32_e32 v17, v16, v17
	v_mul_f32_e32 v34, v16, v34
	v_cvt_pk_bf16_f32 v12, v12, v35
	v_cvt_pk_bf16_f32 v34, v17, v34
	v_lshlrev_b32_e32 v17, 16, v13
	v_and_b32_e32 v35, 0xffff0000, v13
	v_mul_f32_e32 v13, v3, v17
	v_mul_f32_e32 v36, v3, v35
	v_mul_f32_e32 v17, v16, v17
	v_mul_f32_e32 v35, v16, v35
	v_cvt_pk_bf16_f32 v13, v13, v36
	v_cvt_pk_bf16_f32 v35, v17, v35
	v_lshlrev_b32_e32 v17, 16, v14
	v_and_b32_e32 v36, 0xffff0000, v14
	v_mul_f32_e32 v14, v3, v17
	v_mul_f32_e32 v37, v3, v36
	v_mul_f32_e32 v17, v16, v17
	v_mul_f32_e32 v36, v16, v36
	v_cvt_pk_bf16_f32 v14, v14, v37
	v_cvt_pk_bf16_f32 v36, v17, v36
	v_lshlrev_b32_e32 v17, 16, v15
	v_and_b32_e32 v37, 0xffff0000, v15
	v_mul_f32_e32 v15, v3, v17
	v_mul_f32_e32 v3, v3, v37
	v_cvt_pk_bf16_f32 v15, v15, v3
	v_mul_f32_e32 v1, v1, v60
	v_mul_f32_e32 v2, v2, v61
	v_mul_f32_e32 v3, v16, v17
	v_mul_f32_e32 v16, v16, v37
	v_cvt_pk_bf16_f32 v37, v3, v16
	ds_write_b128 v62, v[12:15] offset:16384
	ds_write_b128 v62, v[34:37] offset:32768
	s_waitcnt vmcnt(1)
	ds_write_b128 v63, v[8:11]
	v_exp_f32_e32 v1, v1
	v_exp_f32_e32 v11, v2
	s_waitcnt vmcnt(0)
	v_lshlrev_b32_e32 v3, 16, v4
	v_and_b32_e32 v4, 0xffff0000, v4
	v_mul_f32_e32 v2, v1, v3
	v_mul_f32_e32 v8, v1, v4
	v_mul_f32_e32 v4, v11, v4
	v_cvt_pk_bf16_f32 v2, v2, v8
	v_mul_f32_e32 v3, v11, v3
	v_cvt_pk_bf16_f32 v8, v3, v4
	v_lshlrev_b32_e32 v4, 16, v5
	v_and_b32_e32 v5, 0xffff0000, v5
	v_mul_f32_e32 v3, v1, v4
	v_mul_f32_e32 v9, v1, v5
	v_mul_f32_e32 v5, v11, v5
	v_cvt_pk_bf16_f32 v3, v3, v9
	v_mul_f32_e32 v4, v11, v4
	v_cvt_pk_bf16_f32 v9, v4, v5
	v_lshlrev_b32_e32 v5, 16, v6
	v_and_b32_e32 v6, 0xffff0000, v6
	v_mul_f32_e32 v4, v1, v5
	v_mul_f32_e32 v10, v1, v6
	v_mul_f32_e32 v6, v11, v6
	v_cvt_pk_bf16_f32 v4, v4, v10
	v_mul_f32_e32 v5, v11, v5
	v_cvt_pk_bf16_f32 v10, v5, v6
	v_lshlrev_b32_e32 v6, 16, v7
	v_and_b32_e32 v7, 0xffff0000, v7
	v_mul_f32_e32 v5, v1, v6
	v_mul_f32_e32 v1, v1, v7
	v_cvt_pk_bf16_f32 v5, v5, v1
	v_mul_f32_e32 v1, v11, v6
	v_mul_f32_e32 v6, v11, v7
	v_cvt_pk_bf16_f32 v11, v1, v6
	ds_write_b128 v63, v[2:5] offset:16384
	ds_write_b128 v63, v[8:11] offset:32768
	s_waitcnt lgkmcnt(0)
	s_barrier
	ds_read_b64_tr_b16 v[2:3], v56 offset:0
	ds_read_b64_tr_b16 v[4:5], v56 offset:1024
	ds_read_b64_tr_b16 v[6:7], v57 offset:0
	ds_read_b64_tr_b16 v[8:9], v57 offset:1024
	ds_read_b64_tr_b16 v[34:35], v56 offset:2048
	ds_read_b64_tr_b16 v[36:37], v56 offset:3072
	ds_read_b64_tr_b16 v[64:65], v57 offset:2048
	ds_read_b64_tr_b16 v[66:67], v57 offset:3072
	ds_read_b64_tr_b16 v[72:73], v56 offset:4096
	ds_read_b64_tr_b16 v[74:75], v56 offset:5120
	ds_read_b64_tr_b16 v[76:77], v57 offset:4096
	ds_read_b64_tr_b16 v[78:79], v57 offset:5120
	s_ashr_i32 s18, s18, 2
	s_mul_hi_i32 s19, s18, 0x78787879
	s_lshr_b32 s20, s19, 31
	s_ashr_i32 s19, s19, 4
	s_add_i32 s19, s19, s20
	s_lshl_b32 s17, s17, 1
	s_add_i32 s17, s17, s10
	s_lshl_b32 s20, s19, 3
	s_sub_i32 s17, s17, s19
	s_add_i32 s17, s17, s20
	s_mul_i32 s17, s17, 34
	s_add_i32 s18, s17, s18
	s_waitcnt lgkmcnt(8)
	s_nop 0
	v_mfma_f32_32x32x16_bf16 v[2:17], v[6:9], v[2:5], 0
	ds_read_b64_tr_b16 v[80:81], v56 offset:6144
	ds_read_b64_tr_b16 v[82:83], v56 offset:7168
	ds_read_b64_tr_b16 v[84:85], v57 offset:6144
	ds_read_b64_tr_b16 v[86:87], v57 offset:7168
	s_waitcnt lgkmcnt(8)
	s_nop 0
	v_mfma_f32_32x32x16_bf16 v[2:17], v[64:67], v[34:37], v[2:17]
	ds_read_b64_tr_b16 v[34:35], v56 offset:8192
	ds_read_b64_tr_b16 v[36:37], v56 offset:9216
	ds_read_b64_tr_b16 v[64:65], v57 offset:8192
	ds_read_b64_tr_b16 v[66:67], v57 offset:9216
	s_waitcnt lgkmcnt(8)
	s_nop 0
	v_mfma_f32_32x32x16_bf16 v[2:17], v[76:79], v[72:75], v[2:17]
	ds_read_b64_tr_b16 v[72:73], v56 offset:10240
	ds_read_b64_tr_b16 v[74:75], v56 offset:11264
	ds_read_b64_tr_b16 v[76:77], v57 offset:10240
	ds_read_b64_tr_b16 v[78:79], v57 offset:11264
	s_waitcnt lgkmcnt(8)
	s_nop 0
	v_mfma_f32_32x32x16_bf16 v[2:17], v[84:87], v[80:83], v[2:17]
	ds_read_b64_tr_b16 v[80:81], v56 offset:12288
	ds_read_b64_tr_b16 v[82:83], v56 offset:13312
	ds_read_b64_tr_b16 v[84:85], v57 offset:12288
	ds_read_b64_tr_b16 v[86:87], v57 offset:13312
	s_waitcnt lgkmcnt(8)
	s_nop 0
	v_mfma_f32_32x32x16_bf16 v[2:17], v[64:67], v[34:37], v[2:17]
	ds_read_b64_tr_b16 v[34:35], v56 offset:14336
	ds_read_b64_tr_b16 v[36:37], v56 offset:15360
	ds_read_b64_tr_b16 v[64:65], v57 offset:14336
	ds_read_b64_tr_b16 v[66:67], v57 offset:15360
	s_waitcnt lgkmcnt(8)
	s_nop 0
	v_mfma_f32_32x32x16_bf16 v[2:17], v[76:79], v[72:75], v[2:17]
	s_waitcnt lgkmcnt(4)
	s_nop 0
	v_mfma_f32_32x32x16_bf16 v[2:17], v[84:87], v[80:83], v[2:17]
	s_waitcnt lgkmcnt(0)
	s_nop 0
	v_mfma_f32_32x32x16_bf16 v[2:17], v[64:67], v[34:37], v[2:17]
	s_ashr_i32 s19, s18, 31
	s_nop 15
	s_nop 15
	s_lshl_b64 s[18:19], s[18:19], 13
	v_lshl_add_u64 v[34:35], v[40:41], 0, s[18:19]
	v_cvt_pk_bf16_f32 v2, v2, v3
	v_cvt_pk_bf16_f32 v3, v4, v5
	s_nop 8
	global_store_dwordx2 v[34:35], v[2:3], off
	v_cvt_pk_bf16_f32 v2, v6, v7
	v_cvt_pk_bf16_f32 v3, v8, v9
	global_store_dwordx2 v[34:35], v[2:3], off offset:16
	v_cvt_pk_bf16_f32 v2, v10, v11
	v_cvt_pk_bf16_f32 v3, v12, v13
	global_store_dwordx2 v[34:35], v[2:3], off offset:32
	v_cvt_pk_bf16_f32 v2, v14, v15
	v_cvt_pk_bf16_f32 v3, v16, v17
	global_store_dwordx2 v[34:35], v[2:3], off offset:48
	v_mov_b64_e32 v[12:13], v[18:19]
	v_mov_b64_e32 v[4:5], v[26:27]
	v_mov_b64_e32 v[36:37], v[24:25]
	v_mov_b64_e32 v[8:9], v[30:31]
	s_add_i32 s7, s7, s11
	s_and_b64 vcc, exec, s[14:15]
	v_mov_b64_e32 v[14:15], v[20:21]
	v_mov_b64_e32 v[6:7], v[28:29]
	v_mov_b64_e32 v[34:35], v[22:23]
	v_mov_b64_e32 v[10:11], v[32:33]
	s_mov_b32 s18, s16
	s_barrier
	s_cbranch_vccnz .LBB0_335

.LBB0_477:
	s_add_i32 s2, s58, -2
	s_mul_hi_u32 s3, s2, 0xaaaaaaab
	s_lshr_b32 s3, s3, 2
	s_mul_i32 s3, s3, 6
	s_sub_i32 s2, s2, s3
	s_waitcnt lgkmcnt(0)
	v_mfma_scale_f32_32x32x64_f8f6f4 v[160:175], v[184:191], v[192:199], v[96:111], v207, v218 op_sel_hi:[0,0,0]
	v_mfma_scale_f32_32x32x64_f8f6f4 v[144:159], v[176:183], v[192:199], v[96:111], v207, v218 op_sel_hi:[0,0,0]
	v_cvt_pknorm_u16_f32 v1, v112, v113
	v_cvt_pknorm_u16_f32 v2, v114, v115
	v_perm_b32 v2, v2, v1, s55
	v_cvt_pknorm_u16_f32 v1, v128, v129
	v_cvt_pknorm_u16_f32 v3, v130, v131
	v_perm_b32 v6, v3, v1, s55
	v_cvt_pknorm_u16_f32 v1, v116, v117
	v_cvt_pknorm_u16_f32 v3, v118, v119
	v_perm_b32 v3, v3, v1, s55
	v_cvt_pknorm_u16_f32 v1, v132, v133
	v_cvt_pknorm_u16_f32 v4, v134, v135
	v_perm_b32 v7, v4, v1, s55
	v_cvt_pknorm_u16_f32 v1, v120, v121
	v_cvt_pknorm_u16_f32 v4, v122, v123
	v_perm_b32 v4, v4, v1, s55
	v_cvt_pknorm_u16_f32 v1, v136, v137
	v_cvt_pknorm_u16_f32 v5, v138, v139
	v_perm_b32 v8, v5, v1, s55
	v_cvt_pknorm_u16_f32 v1, v124, v125
	v_cvt_pknorm_u16_f32 v5, v126, v127
	v_perm_b32 v5, v5, v1, s55
	v_cvt_pknorm_u16_f32 v1, v140, v141
	v_cvt_pknorm_u16_f32 v9, v142, v143
	v_perm_b32 v9, v9, v1, s55
	s_mulk_i32 s2, 0x2800
	s_add_i32 s2, s10, s2
	v_add_u32_e32 v1, s2, v208
	s_nop 4
	v_add_u32_e32 v10, v1, v209
	v_add_u32_e32 v1, v1, v217
	ds_read_b128 v[96:99], v10
	ds_read_b128 v[100:103], v1
	ds_read_b128 v[104:107], v10 offset:2048
	ds_read_b128 v[108:111], v1 offset:2048
	ds_read_b128 v[112:115], v10 offset:4096
	ds_read_b128 v[116:119], v1 offset:4096
	ds_read_b128 v[120:123], v10 offset:6144
	ds_read_b128 v[124:127], v1 offset:6144
	ds_read_b128 v[128:131], v10 offset:8192
	ds_read_b128 v[132:135], v1 offset:8192
	s_waitcnt lgkmcnt(8)
	v_mfma_scale_f32_32x32x64_f8f6f4 v[64:79], v[96:103], v[2:9], v[64:79], v207, v207 op_sel_hi:[0,0,0]
	s_waitcnt lgkmcnt(6)
	v_mfma_scale_f32_32x32x64_f8f6f4 v[48:63], v[104:111], v[2:9], v[48:63], v207, v207 op_sel_hi:[0,0,0]
	s_waitcnt lgkmcnt(4)
	v_mfma_scale_f32_32x32x64_f8f6f4 v[32:47], v[112:119], v[2:9], v[32:47], v207, v207 op_sel_hi:[0,0,0]
	s_waitcnt lgkmcnt(2)
	v_mfma_scale_f32_32x32x64_f8f6f4 v[16:31], v[120:127], v[2:9], v[16:31], v207, v207 op_sel_hi:[0,0,0]
	s_waitcnt lgkmcnt(0)
	v_mfma_scale_f32_32x32x64_f8f6f4 v[80:95], v[128:135], v[2:9], v[80:95], v207, v207 op_sel_hi:[0,0,0]
	v_max_f32_e32 v1, v161, v161
	v_max_f32_e32 v2, v160, v160
	v_max_f32_e32 v1, v2, v1
	v_max3_f32 v1, v1, v162, v163
	v_max3_f32 v1, v1, v164, v165
	v_max3_f32 v1, v1, v166, v167
	v_max3_f32 v1, v1, v168, v169
	v_max3_f32 v1, v1, v170, v171
	v_max3_f32 v1, v1, v172, v173
	v_max3_f32 v1, v1, v174, v175
	v_max3_f32 v1, v1, v144, v145
	v_max3_f32 v1, v1, v146, v147
	v_max3_f32 v1, v1, v148, v149
	v_max3_f32 v1, v1, v150, v151
	v_max3_f32 v1, v1, v152, v153
	v_max3_f32 v1, v1, v154, v155
	v_max3_f32 v1, v1, v156, v157
	v_max3_f32 v1, v1, v158, v159
	v_mov_b32_e32 v2, v1
	s_nop 1
	v_permlane32_swap_b32_e32 v1, v2
	v_max_f32_e32 v2, v2, v2
	v_max_f32_e32 v1, v1, v1
	v_max_f32_e32 v1, v1, v2
	v_cmp_ge_f32_e32 vcc, s53, v1
	v_mov_b32_e32 v2, 1.0
	s_cmp_eq_u64 vcc, exec
	s_cbranch_scc0 .LBB0_485
	v_cmp_gt_f32_e32 vcc, 1.0, v2
	s_cbranch_vccz .LBB0_480

.LBB0_480:
	v_cvt_pknorm_u16_f32 v1, v160, v161
	v_cvt_pknorm_u16_f32 v2, v162, v163
	v_perm_b32 v2, v2, v1, s55
	v_cvt_pknorm_u16_f32 v1, v144, v145
	v_cvt_pknorm_u16_f32 v3, v146, v147
	v_perm_b32 v6, v3, v1, s55
	v_cvt_pknorm_u16_f32 v1, v164, v165
	v_cvt_pknorm_u16_f32 v3, v166, v167
	v_perm_b32 v3, v3, v1, s55
	v_cvt_pknorm_u16_f32 v1, v148, v149
	v_cvt_pknorm_u16_f32 v4, v150, v151
	v_perm_b32 v7, v4, v1, s55
	v_cvt_pknorm_u16_f32 v1, v168, v169
	v_cvt_pknorm_u16_f32 v4, v170, v171
	s_mul_hi_u32 s2, s17, 0xaaaaaaab
	v_perm_b32 v4, v4, v1, s55
	v_cvt_pknorm_u16_f32 v1, v152, v153
	v_cvt_pknorm_u16_f32 v5, v154, v155
	s_lshr_b32 s2, s2, 2
	v_perm_b32 v8, v5, v1, s55
	v_cvt_pknorm_u16_f32 v1, v172, v173
	v_cvt_pknorm_u16_f32 v5, v174, v175
	s_mul_i32 s2, s2, 6
	v_perm_b32 v5, v5, v1, s55
	v_cvt_pknorm_u16_f32 v1, v156, v157
	v_cvt_pknorm_u16_f32 v9, v158, v159
	s_sub_i32 s2, s17, s2
	v_perm_b32 v9, v9, v1, s55
	s_mulk_i32 s2, 0x2800
	s_add_i32 s2, s10, s2
	v_add_u32_e32 v1, s2, v208
	s_nop 4
	v_add_u32_e32 v10, v1, v209
	v_add_u32_e32 v1, v1, v217
	ds_read_b128 v[96:99], v10
	ds_read_b128 v[100:103], v1
	ds_read_b128 v[104:107], v10 offset:2048
	ds_read_b128 v[108:111], v1 offset:2048
	ds_read_b128 v[112:115], v10 offset:4096
	ds_read_b128 v[116:119], v1 offset:4096
	ds_read_b128 v[120:123], v10 offset:6144
	ds_read_b128 v[124:127], v1 offset:6144
	ds_read_b128 v[128:131], v10 offset:8192
	ds_read_b128 v[132:135], v1 offset:8192
	s_mov_b32 s2, s47
	s_waitcnt lgkmcnt(8)
	v_mfma_scale_f32_32x32x64_f8f6f4 v[64:79], v[96:103], v[2:9], v[64:79], v207, v207 op_sel_hi:[0,0,0]
	s_waitcnt lgkmcnt(6)
	v_mfma_scale_f32_32x32x64_f8f6f4 v[48:63], v[104:111], v[2:9], v[48:63], v207, v207 op_sel_hi:[0,0,0]
	s_waitcnt lgkmcnt(4)
	v_mfma_scale_f32_32x32x64_f8f6f4 v[32:47], v[112:119], v[2:9], v[32:47], v207, v207 op_sel_hi:[0,0,0]
	s_waitcnt lgkmcnt(2)
	v_mfma_scale_f32_32x32x64_f8f6f4 v[16:31], v[120:127], v[2:9], v[16:31], v207, v207 op_sel_hi:[0,0,0]
	s_waitcnt lgkmcnt(0)
	v_mfma_scale_f32_32x32x64_f8f6f4 v[80:95], v[128:135], v[2:9], v[80:95], v207, v207 op_sel_hi:[0,0,0]
	s_nop 0
	s_nop 15
	s_nop 15
	v_mbcnt_lo_u32_b32 v2, -1, 0
	v_mbcnt_hi_u32_b32 v2, -1, v2
	s_waitcnt vmcnt(0)
	s_waitcnt vmcnt(0)
	v_lshl_add_u32 v3, s2, 6, v2
	v_and_b32_e32 v252, 15, v2
	v_lshlrev_b32_e32 v252, 2, v252
	ds_bpermute_b32 v253, v252, v248
	ds_bpermute_b32 v254, v252, v249
	v_and_b32_e32 v1, 16, v2
	v_cmp_ne_u32_e32 vcc, 0, v1
	s_waitcnt lgkmcnt(0)
	s_nop 0
	v_cndmask_b32_e32 v253, v253, v254, vcc
	v_add_f32_e32 v80, v80, v253
	v_rcp_f32_e32 v1, v80
	v_lshlrev_b32_e32 v5, 8, v3
	v_and_b32_e32 v5, 0xc000, v5
	v_and_b32_e32 v4, 63, v2
	v_add_u32_e32 v5, s10, v5
	v_and_b32_e32 v6, 0xffffff00, v3
	v_cmp_eq_u32_e32 vcc, s71, v6
	v_lshl_add_u32 v14, v4, 2, v5
	s_barrier
	s_and_saveexec_b64 s[4:5], vcc
	s_cbranch_execz .LBB0_482
	v_mul_f32_e32 v4, v206, v1
	v_mul_f32_e32 v5, v64, v4
	v_mul_f32_e32 v6, v65, v4
	ds_write2st64_b32 v14, v5, v6 offset1:1
	v_mul_f32_e32 v5, v66, v4
	v_mul_f32_e32 v6, v67, v4
	ds_write2st64_b32 v14, v5, v6 offset0:2 offset1:3
	v_mul_f32_e32 v5, v68, v4
	v_mul_f32_e32 v6, v69, v4
	ds_write2st64_b32 v14, v5, v6 offset0:4 offset1:5
	v_mul_f32_e32 v5, v70, v4
	v_mul_f32_e32 v6, v71, v4
	ds_write2st64_b32 v14, v5, v6 offset0:6 offset1:7
	v_mul_f32_e32 v5, v72, v4
	v_mul_f32_e32 v6, v73, v4
	ds_write2st64_b32 v14, v5, v6 offset0:8 offset1:9
	v_mul_f32_e32 v5, v74, v4
	v_mul_f32_e32 v6, v75, v4
	ds_write2st64_b32 v14, v5, v6 offset0:10 offset1:11
	v_mul_f32_e32 v5, v76, v4
	v_mul_f32_e32 v6, v77, v4
	ds_write2st64_b32 v14, v5, v6 offset0:12 offset1:13
	v_mul_f32_e32 v5, v78, v4
	v_mul_f32_e32 v6, v79, v4
	ds_write2st64_b32 v14, v5, v6 offset0:14 offset1:15
	v_mul_f32_e32 v5, v48, v4
	v_mul_f32_e32 v6, v49, v4
	ds_write2st64_b32 v14, v5, v6 offset0:16 offset1:17
	v_mul_f32_e32 v5, v50, v4
	v_mul_f32_e32 v6, v51, v4
	ds_write2st64_b32 v14, v5, v6 offset0:18 offset1:19
	v_mul_f32_e32 v5, v52, v4
	v_mul_f32_e32 v6, v53, v4
	ds_write2st64_b32 v14, v5, v6 offset0:20 offset1:21
	v_mul_f32_e32 v5, v54, v4
	v_mul_f32_e32 v6, v55, v4
	ds_write2st64_b32 v14, v5, v6 offset0:22 offset1:23
	v_mul_f32_e32 v5, v56, v4
	v_mul_f32_e32 v6, v57, v4
	ds_write2st64_b32 v14, v5, v6 offset0:24 offset1:25
	v_mul_f32_e32 v5, v58, v4
	v_mul_f32_e32 v6, v59, v4
	ds_write2st64_b32 v14, v5, v6 offset0:26 offset1:27
	v_mul_f32_e32 v5, v60, v4
	v_mul_f32_e32 v6, v61, v4
	ds_write2st64_b32 v14, v5, v6 offset0:28 offset1:29
	v_mul_f32_e32 v5, v62, v4
	v_mul_f32_e32 v6, v63, v4
	ds_write2st64_b32 v14, v5, v6 offset0:30 offset1:31
	v_mul_f32_e32 v5, v32, v4
	v_mul_f32_e32 v6, v33, v4
	ds_write2st64_b32 v14, v5, v6 offset0:32 offset1:33
	v_mul_f32_e32 v5, v34, v4
	v_mul_f32_e32 v6, v35, v4
	ds_write2st64_b32 v14, v5, v6 offset0:34 offset1:35
	v_mul_f32_e32 v5, v36, v4
	v_mul_f32_e32 v6, v37, v4
	ds_write2st64_b32 v14, v5, v6 offset0:36 offset1:37
	v_mul_f32_e32 v5, v38, v4
	v_mul_f32_e32 v6, v39, v4
	ds_write2st64_b32 v14, v5, v6 offset0:38 offset1:39
	v_mul_f32_e32 v5, v40, v4
	v_mul_f32_e32 v6, v41, v4
	ds_write2st64_b32 v14, v5, v6 offset0:40 offset1:41
	v_mul_f32_e32 v5, v42, v4
	v_mul_f32_e32 v6, v43, v4
	ds_write2st64_b32 v14, v5, v6 offset0:42 offset1:43
	v_mul_f32_e32 v5, v44, v4
	v_mul_f32_e32 v6, v45, v4
	ds_write2st64_b32 v14, v5, v6 offset0:44 offset1:45
	v_mul_f32_e32 v5, v46, v4
	v_mul_f32_e32 v6, v47, v4
	ds_write2st64_b32 v14, v5, v6 offset0:46 offset1:47
	v_mul_f32_e32 v5, v16, v4
	v_mul_f32_e32 v6, v17, v4
	ds_write2st64_b32 v14, v5, v6 offset0:48 offset1:49
	v_mul_f32_e32 v5, v18, v4
	v_mul_f32_e32 v6, v19, v4
	ds_write2st64_b32 v14, v5, v6 offset0:50 offset1:51
	v_mul_f32_e32 v5, v20, v4
	v_mul_f32_e32 v6, v21, v4
	ds_write2st64_b32 v14, v5, v6 offset0:52 offset1:53
	v_mul_f32_e32 v5, v22, v4
	v_mul_f32_e32 v6, v23, v4
	ds_write2st64_b32 v14, v5, v6 offset0:54 offset1:55
	v_mul_f32_e32 v5, v24, v4
	v_mul_f32_e32 v6, v25, v4
	ds_write2st64_b32 v14, v5, v6 offset0:56 offset1:57
	v_mul_f32_e32 v5, v26, v4
	v_mul_f32_e32 v6, v27, v4
	ds_write2st64_b32 v14, v5, v6 offset0:58 offset1:59
	v_mul_f32_e32 v5, v28, v4
	v_mul_f32_e32 v6, v29, v4
	ds_write2st64_b32 v14, v5, v6 offset0:60 offset1:61
	v_mul_f32_e32 v5, v30, v4
	v_mul_f32_e32 v4, v31, v4
	ds_write2st64_b32 v14, v5, v4 offset0:62 offset1:63

.LBB0_695:
	v_mov_b32_e32 v163, v0
	v_mov_b32_e32 v167, v0
	s_add_u32 s11, s22, 0x100
	s_waitcnt vmcnt(0)
	s_addc_u32 s93, s23, 0
	v_lshl_add_u64 v[170:171], s[88:89], 0, v[166:167]
	v_lshl_add_u64 v[172:173], s[88:89], 0, v[162:163]
	s_mov_b32 s14, -2
	s_mov_b64 s[96:97], 0
	v_add_u32_e32 v2, s45, v223
	v_add_u32_e32 v14, s50, v223
	s_add_u32 s22, s96, 0x100
	ds_read_b128 v[18:21], v2
	ds_read_b128 v[22:25], v2 offset:1024
	ds_read_b128 v[26:29], v2 offset:2048
	ds_read_b128 v[30:33], v2 offset:3072
	ds_read_b128 v[2:5], v14
	ds_read_b128 v[6:9], v14 offset:1024
	ds_read_b128 v[10:13], v14 offset:2048
	ds_read_b128 v[14:17], v14 offset:3072
	s_addc_u32 s23, s97, 0
	s_add_u32 s15, s11, s96
	s_addc_u32 s94, s93, s97
	s_cmpk_eq_i32 s96, 0x300
	s_cselect_b64 vcc, -1, 0
	s_and_b64 s[62:63], vcc, exec
	v_cndmask_b32_e32 v180, v164, v226, vcc
	v_cndmask_b32_e32 v178, v168, v227, vcc
	v_cndmask_b32_e32 v163, v162, v228, vcc
	v_cndmask_b32_e32 v165, v166, v229, vcc
	s_cselect_b32 s95, s7, s94
	s_cselect_b32 s94, s6, s15
	s_cselect_b32 s15, 0, s22
	v_lshl_add_u64 v[174:175], v[172:173], 0, s[96:97]
	s_add_i32 m0, s54, 0xc000
	ds_read_b128 v[192:195], v225
	ds_read_b128 v[196:199], v225 offset:1024
	ds_read_b128 v[200:203], v225 offset:2048
	ds_read_b128 v[204:207], v225 offset:3072
	ds_read_b128 v[230:233], v225 offset:4096
	ds_read_b128 v[234:237], v225 offset:5120
	ds_read_b128 v[238:241], v225 offset:6144
	ds_read_b128 v[242:245], v225 offset:7168
	global_load_lds_dwordx4 v[174:175], off
	v_lshl_add_u64 v[174:175], v[170:171], 0, s[96:97]
	s_add_i32 m0, s54, 0xe000
	s_nop 0
	global_load_lds_dwordx4 v[174:175], off
	s_waitcnt vmcnt(8)
	s_waitcnt lgkmcnt(0)
	s_barrier
	s_setprio 1
	s_waitcnt lgkmcnt(0)
	v_mfma_scale_f32_16x16x128_f8f6f4 v[158:161], v[18:25], v[192:199], 0, v220, v220 op_sel_hi:[0,0,0]
	v_mfma_scale_f32_16x16x128_f8f6f4 v[154:157], v[26:33], v[192:199], 0, v220, v220 op_sel_hi:[0,0,0]
	v_mfma_scale_f32_16x16x128_f8f6f4 v[142:145], v[18:25], v[200:207], 0, v220, v220 op_sel_hi:[0,0,0]
	v_mfma_scale_f32_16x16x128_f8f6f4 v[138:141], v[26:33], v[200:207], 0, v220, v220 op_sel_hi:[0,0,0]
	v_mfma_scale_f32_16x16x128_f8f6f4 v[126:129], v[18:25], v[230:237], 0, v220, v220 op_sel_hi:[0,0,0]
	v_mfma_scale_f32_16x16x128_f8f6f4 v[122:125], v[26:33], v[230:237], 0, v220, v220 op_sel_hi:[0,0,0]
	v_mfma_scale_f32_16x16x128_f8f6f4 v[110:113], v[18:25], v[238:245], 0, v220, v220 op_sel_hi:[0,0,0]
	v_mfma_scale_f32_16x16x128_f8f6f4 v[106:109], v[26:33], v[238:245], 0, v220, v220 op_sel_hi:[0,0,0]
	s_setprio 0
	s_setprio 1
	v_mfma_scale_f32_16x16x128_f8f6f4 v[150:153], v[2:9], v[192:199], 0, v220, v220 op_sel_hi:[0,0,0]
	v_mfma_scale_f32_16x16x128_f8f6f4 v[146:149], v[10:17], v[192:199], 0, v220, v220 op_sel_hi:[0,0,0]
	v_mfma_scale_f32_16x16x128_f8f6f4 v[134:137], v[2:9], v[200:207], 0, v220, v220 op_sel_hi:[0,0,0]
	v_mfma_scale_f32_16x16x128_f8f6f4 v[130:133], v[10:17], v[200:207], 0, v220, v220 op_sel_hi:[0,0,0]
	v_mfma_scale_f32_16x16x128_f8f6f4 v[118:121], v[2:9], v[230:237], 0, v220, v220 op_sel_hi:[0,0,0]
	v_mfma_scale_f32_16x16x128_f8f6f4 v[114:117], v[10:17], v[230:237], 0, v220, v220 op_sel_hi:[0,0,0]
	v_mfma_scale_f32_16x16x128_f8f6f4 v[102:105], v[2:9], v[238:245], 0, v220, v220 op_sel_hi:[0,0,0]
	v_mfma_scale_f32_16x16x128_f8f6f4 v[98:101], v[10:17], v[238:245], 0, v220, v220 op_sel_hi:[0,0,0]
	s_setprio 0
	s_barrier
	s_mov_b32 m0, s48
	v_lshl_add_u64 v[174:175], s[94:95], 0, v[186:187]
	s_add_u32 s62, s94, 0x20000
	ds_read_b128 v[192:195], v225 offset:16384
	ds_read_b128 v[196:199], v225 offset:17408
	ds_read_b128 v[200:203], v225 offset:18432
	ds_read_b128 v[204:207], v225 offset:19456
	ds_read_b128 v[230:233], v225 offset:20480
	ds_read_b128 v[234:237], v225 offset:21504
	ds_read_b128 v[238:241], v225 offset:22528
	ds_read_b128 v[242:245], v225 offset:23552
	global_load_lds_dwordx4 v[174:175], off
	v_lshl_add_u64 v[176:177], s[94:95], 0, v[188:189]
	s_mov_b32 m0, s49
	s_addc_u32 s63, s95, 0
	global_load_lds_dwordx4 v[176:177], off
	v_lshl_add_u64 v[182:183], s[62:63], 0, v[186:187]
	s_mov_b32 m0, s51
	s_add_u32 s96, s84, s15
	global_load_lds_dwordx4 v[182:183], off
	v_lshl_add_u64 v[182:183], s[62:63], 0, v[188:189]
	s_mov_b32 m0, s52
	s_addc_u32 s97, s85, 0
	global_load_lds_dwordx4 v[182:183], off
	s_mov_b32 m0, s54
	v_mov_b32_e32 v181, v0
	global_load_lds_dwordx4 v180, s[96:97]
	s_mov_b32 m0, s56
	v_mov_b32_e32 v179, v0
	global_load_lds_dwordx4 v178, s[96:97]
	s_waitcnt vmcnt(8)
	s_waitcnt lgkmcnt(0)
	v_lshl_add_u64 v[180:181], s[96:97], 0, v[180:181]
	v_lshl_add_u64 v[178:179], s[96:97], 0, v[178:179]
	s_barrier
	s_setprio 1
	s_waitcnt lgkmcnt(0)
	v_mfma_scale_f32_16x16x128_f8f6f4 v[94:97], v[18:25], v[192:199], 0, v220, v220 op_sel_hi:[0,0,0]
	v_mfma_scale_f32_16x16x128_f8f6f4 v[90:93], v[26:33], v[192:199], 0, v220, v220 op_sel_hi:[0,0,0]
	v_mfma_scale_f32_16x16x128_f8f6f4 v[78:81], v[18:25], v[200:207], 0, v220, v220 op_sel_hi:[0,0,0]
	v_mfma_scale_f32_16x16x128_f8f6f4 v[74:77], v[26:33], v[200:207], 0, v220, v220 op_sel_hi:[0,0,0]
	v_mfma_scale_f32_16x16x128_f8f6f4 v[58:61], v[18:25], v[230:237], 0, v220, v220 op_sel_hi:[0,0,0]
	v_mfma_scale_f32_16x16x128_f8f6f4 v[42:45], v[26:33], v[230:237], 0, v220, v220 op_sel_hi:[0,0,0]
	v_mfma_scale_f32_16x16x128_f8f6f4 v[38:41], v[18:25], v[238:245], 0, v220, v220 op_sel_hi:[0,0,0]
	v_mfma_scale_f32_16x16x128_f8f6f4 v[34:37], v[26:33], v[238:245], 0, v220, v220 op_sel_hi:[0,0,0]
	s_setprio 0
	s_setprio 1
	v_mfma_scale_f32_16x16x128_f8f6f4 v[86:89], v[2:9], v[192:199], 0, v220, v220 op_sel_hi:[0,0,0]
	v_mfma_scale_f32_16x16x128_f8f6f4 v[82:85], v[10:17], v[192:199], 0, v220, v220 op_sel_hi:[0,0,0]
	v_mfma_scale_f32_16x16x128_f8f6f4 v[62:65], v[2:9], v[200:207], 0, v220, v220 op_sel_hi:[0,0,0]
	v_mfma_scale_f32_16x16x128_f8f6f4 v[50:53], v[10:17], v[200:207], 0, v220, v220 op_sel_hi:[0,0,0]
	v_mfma_scale_f32_16x16x128_f8f6f4 v[70:73], v[2:9], v[230:237], 0, v220, v220 op_sel_hi:[0,0,0]
	v_mfma_scale_f32_16x16x128_f8f6f4 v[66:69], v[10:17], v[230:237], 0, v220, v220 op_sel_hi:[0,0,0]
	v_mfma_scale_f32_16x16x128_f8f6f4 v[54:57], v[2:9], v[238:245], 0, v220, v220 op_sel_hi:[0,0,0]
	v_mfma_scale_f32_16x16x128_f8f6f4 v[46:49], v[10:17], v[238:245], 0, v220, v220 op_sel_hi:[0,0,0]
	s_setprio 0
	s_barrier
	v_add_u32_e32 v14, s65, v223
	v_add_u32_e32 v30, s70, v223
	ds_read_b128 v[2:5], v14
	ds_read_b128 v[6:9], v14 offset:1024
	ds_read_b128 v[10:13], v14 offset:2048
	ds_read_b128 v[14:17], v14 offset:3072
	ds_read_b128 v[18:21], v30
	ds_read_b128 v[22:25], v30 offset:1024
	ds_read_b128 v[26:29], v30 offset:2048
	ds_read_b128 v[30:33], v30 offset:3072
	s_mov_b32 m0, s58
	ds_read_b128 v[192:195], v225 offset:32768
	ds_read_b128 v[196:199], v225 offset:33792
	ds_read_b128 v[200:203], v225 offset:34816
	ds_read_b128 v[204:207], v225 offset:35840
	ds_read_b128 v[230:233], v225 offset:36864
	ds_read_b128 v[234:237], v225 offset:37888
	ds_read_b128 v[238:241], v225 offset:38912
	ds_read_b128 v[242:245], v225 offset:39936
	global_load_lds_dwordx4 v163, s[96:97]
	s_mov_b32 m0, s59
	s_nop 0
	global_load_lds_dwordx4 v165, s[96:97]
	s_waitcnt vmcnt(8)
	s_waitcnt lgkmcnt(0)
	s_barrier
	s_setprio 1
	s_waitcnt lgkmcnt(0)
	v_mfma_scale_f32_16x16x128_f8f6f4 v[158:161], v[2:9], v[192:199], v[158:161], v220, v220 op_sel_hi:[0,0,0]
	v_mfma_scale_f32_16x16x128_f8f6f4 v[154:157], v[10:17], v[192:199], v[154:157], v220, v220 op_sel_hi:[0,0,0]
	v_mfma_scale_f32_16x16x128_f8f6f4 v[142:145], v[2:9], v[200:207], v[142:145], v220, v220 op_sel_hi:[0,0,0]
	v_mfma_scale_f32_16x16x128_f8f6f4 v[138:141], v[10:17], v[200:207], v[138:141], v220, v220 op_sel_hi:[0,0,0]
	v_mfma_scale_f32_16x16x128_f8f6f4 v[126:129], v[2:9], v[230:237], v[126:129], v220, v220 op_sel_hi:[0,0,0]
	v_mfma_scale_f32_16x16x128_f8f6f4 v[122:125], v[10:17], v[230:237], v[122:125], v220, v220 op_sel_hi:[0,0,0]
	v_mfma_scale_f32_16x16x128_f8f6f4 v[110:113], v[2:9], v[238:245], v[110:113], v220, v220 op_sel_hi:[0,0,0]
	v_mfma_scale_f32_16x16x128_f8f6f4 v[106:109], v[10:17], v[238:245], v[106:109], v220, v220 op_sel_hi:[0,0,0]
	s_setprio 0
	s_setprio 1
	v_mfma_scale_f32_16x16x128_f8f6f4 v[150:153], v[18:25], v[192:199], v[150:153], v220, v220 op_sel_hi:[0,0,0]
	v_mfma_scale_f32_16x16x128_f8f6f4 v[146:149], v[26:33], v[192:199], v[146:149], v220, v220 op_sel_hi:[0,0,0]
	v_mfma_scale_f32_16x16x128_f8f6f4 v[134:137], v[18:25], v[200:207], v[134:137], v220, v220 op_sel_hi:[0,0,0]
	v_mfma_scale_f32_16x16x128_f8f6f4 v[130:133], v[26:33], v[200:207], v[130:133], v220, v220 op_sel_hi:[0,0,0]
	v_mfma_scale_f32_16x16x128_f8f6f4 v[118:121], v[18:25], v[230:237], v[118:121], v220, v220 op_sel_hi:[0,0,0]
	v_mfma_scale_f32_16x16x128_f8f6f4 v[114:117], v[26:33], v[230:237], v[114:117], v220, v220 op_sel_hi:[0,0,0]
	v_mfma_scale_f32_16x16x128_f8f6f4 v[102:105], v[18:25], v[238:245], v[102:105], v220, v220 op_sel_hi:[0,0,0]
	v_mfma_scale_f32_16x16x128_f8f6f4 v[98:101], v[26:33], v[238:245], v[98:101], v220, v220 op_sel_hi:[0,0,0]
	s_setprio 0
	s_barrier
	s_mov_b32 m0, s66
	v_lshl_add_u64 v[174:175], v[174:175], 0, s[38:39]
	s_add_u32 s62, s94, 0x20080
	ds_read_b128 v[192:195], v225 offset:49152
	ds_read_b128 v[196:199], v225 offset:50176
	ds_read_b128 v[200:203], v225 offset:51200
	ds_read_b128 v[204:207], v225 offset:52224
	ds_read_b128 v[230:233], v225 offset:53248
	ds_read_b128 v[234:237], v225 offset:54272
	ds_read_b128 v[238:241], v225 offset:55296
	ds_read_b128 v[242:245], v225 offset:56320
	global_load_lds_dwordx4 v[174:175], off
	v_lshl_add_u64 v[174:175], v[176:177], 0, s[38:39]
	s_mov_b32 m0, s67
	s_addc_u32 s63, s95, 0
	global_load_lds_dwordx4 v[174:175], off
	v_lshl_add_u64 v[174:175], s[62:63], 0, v[186:187]
	s_mov_b32 m0, s71
	s_nop 0
	global_load_lds_dwordx4 v[174:175], off
	v_lshl_add_u64 v[174:175], s[62:63], 0, v[188:189]
	s_mov_b32 m0, s72
	s_nop 0
	global_load_lds_dwordx4 v[174:175], off
	v_lshl_add_u64 v[174:175], v[180:181], 0, s[38:39]
	s_mov_b32 m0, s68
	s_nop 0
	global_load_lds_dwordx4 v[174:175], off
	v_lshl_add_u64 v[174:175], v[178:179], 0, s[38:39]
	s_mov_b32 m0, s69
	s_nop 0
	global_load_lds_dwordx4 v[174:175], off
	s_waitcnt vmcnt(8)
	s_waitcnt lgkmcnt(0)
	s_barrier
	s_setprio 1
	s_waitcnt lgkmcnt(0)
	v_mfma_scale_f32_16x16x128_f8f6f4 v[94:97], v[2:9], v[192:199], v[94:97], v220, v220 op_sel_hi:[0,0,0]
	v_mfma_scale_f32_16x16x128_f8f6f4 v[90:93], v[10:17], v[192:199], v[90:93], v220, v220 op_sel_hi:[0,0,0]
	v_mfma_scale_f32_16x16x128_f8f6f4 v[78:81], v[2:9], v[200:207], v[78:81], v220, v220 op_sel_hi:[0,0,0]
	v_mfma_scale_f32_16x16x128_f8f6f4 v[74:77], v[10:17], v[200:207], v[74:77], v220, v220 op_sel_hi:[0,0,0]
	v_mfma_scale_f32_16x16x128_f8f6f4 v[58:61], v[2:9], v[230:237], v[58:61], v220, v220 op_sel_hi:[0,0,0]
	v_mfma_scale_f32_16x16x128_f8f6f4 v[42:45], v[10:17], v[230:237], v[42:45], v220, v220 op_sel_hi:[0,0,0]
	v_mfma_scale_f32_16x16x128_f8f6f4 v[38:41], v[2:9], v[238:245], v[38:41], v220, v220 op_sel_hi:[0,0,0]
	v_mfma_scale_f32_16x16x128_f8f6f4 v[34:37], v[10:17], v[238:245], v[34:37], v220, v220 op_sel_hi:[0,0,0]
	s_setprio 0
	s_setprio 1
	v_mfma_scale_f32_16x16x128_f8f6f4 v[86:89], v[18:25], v[192:199], v[86:89], v220, v220 op_sel_hi:[0,0,0]
	v_mfma_scale_f32_16x16x128_f8f6f4 v[82:85], v[26:33], v[192:199], v[82:85], v220, v220 op_sel_hi:[0,0,0]
	v_mfma_scale_f32_16x16x128_f8f6f4 v[62:65], v[18:25], v[200:207], v[62:65], v220, v220 op_sel_hi:[0,0,0]
	v_mfma_scale_f32_16x16x128_f8f6f4 v[50:53], v[26:33], v[200:207], v[50:53], v220, v220 op_sel_hi:[0,0,0]
	v_mfma_scale_f32_16x16x128_f8f6f4 v[70:73], v[18:25], v[230:237], v[70:73], v220, v220 op_sel_hi:[0,0,0]
	v_mfma_scale_f32_16x16x128_f8f6f4 v[66:69], v[26:33], v[230:237], v[66:69], v220, v220 op_sel_hi:[0,0,0]
	v_mfma_scale_f32_16x16x128_f8f6f4 v[54:57], v[18:25], v[238:245], v[54:57], v220, v220 op_sel_hi:[0,0,0]
	v_mfma_scale_f32_16x16x128_f8f6f4 v[46:49], v[26:33], v[238:245], v[46:49], v220, v220 op_sel_hi:[0,0,0]
	s_setprio 0
	s_barrier
	s_add_i32 s14, s14, 2
	s_cmp_gt_u32 s14, 5
	s_mov_b64 s[96:97], s[22:23]

.LBB0_1056:
	s_lshl_b32 s18, s18, 4
	s_ashr_i32 s19, s18, 31
	s_lshl_b64 s[18:19], s[18:19], 2
	v_mov_b32_e32 v169, v0
	v_mov_b32_e32 v171, v0
	s_add_u32 s90, s65, s18
	s_addc_u32 s91, s66, s19
	v_lshl_add_u64 v[176:177], v[2:3], 0, s[42:43]
	v_lshl_add_u64 v[178:179], s[16:17], 0, v[170:171]
	v_lshl_add_u64 v[180:181], s[16:17], 0, v[168:169]
	s_mov_b32 s23, -2
	s_mov_b64 s[94:95], 0
	s_mov_b64 s[96:97], s[94:95]
	s_add_u32 s94, s96, 0x100
	s_addc_u32 s95, s97, 0
	s_cmpk_eq_i32 s96, 0x300
	v_lshl_add_u64 v[2:3], v[176:177], 0, s[96:97]
	s_cselect_b64 vcc, -1, 0
	v_cndmask_b32_e32 v182, v2, v166, vcc
	v_add_u32_e32 v2, s26, v197
	v_add_u32_e32 v14, s45, v197
	v_cndmask_b32_e32 v183, v3, v167, vcc
	ds_read_b128 v[18:21], v2
	ds_read_b128 v[22:25], v2 offset:1024
	ds_read_b128 v[26:29], v2 offset:2048
	ds_read_b128 v[30:33], v2 offset:3072
	ds_read_b128 v[2:5], v14
	ds_read_b128 v[6:9], v14 offset:1024
	ds_read_b128 v[10:13], v14 offset:2048
	ds_read_b128 v[14:17], v14 offset:3072
	s_and_b64 s[18:19], vcc, exec
	v_cndmask_b32_e32 v190, v172, v200, vcc
	v_cndmask_b32_e32 v188, v174, v202, vcc
	v_cndmask_b32_e32 v171, v168, v201, vcc
	v_cndmask_b32_e32 v169, v170, v203, vcc
	s_cselect_b32 s18, 0, s94
	v_lshl_add_u64 v[184:185], v[180:181], 0, s[96:97]
	s_add_i32 m0, s50, 0xc000
	ds_read_b128 v[218:221], v175
	ds_read_b128 v[222:225], v175 offset:1024
	ds_read_b128 v[226:229], v175 offset:2048
	ds_read_b128 v[230:233], v175 offset:3072
	ds_read_b128 v[234:237], v175 offset:4096
	ds_read_b128 v[238:241], v175 offset:5120
	ds_read_b128 v[242:245], v175 offset:6144
	ds_read_b128 v[246:249], v175 offset:7168
	global_load_lds_dwordx4 v[184:185], off
	v_lshl_add_u64 v[184:185], v[178:179], 0, s[96:97]
	s_add_i32 m0, s50, 0xe000
	s_nop 0
	global_load_lds_dwordx4 v[184:185], off
	s_waitcnt vmcnt(8)
	s_waitcnt lgkmcnt(0)
	s_barrier
	s_setprio 1
	s_waitcnt lgkmcnt(0)
	v_mfma_scale_f32_16x16x128_f8f6f4 v[158:161], v[18:25], v[218:225], 0, v193, v193 op_sel_hi:[0,0,0]
	v_mfma_scale_f32_16x16x128_f8f6f4 v[154:157], v[26:33], v[218:225], 0, v193, v193 op_sel_hi:[0,0,0]
	v_mfma_scale_f32_16x16x128_f8f6f4 v[142:145], v[18:25], v[226:233], 0, v193, v193 op_sel_hi:[0,0,0]
	v_mfma_scale_f32_16x16x128_f8f6f4 v[138:141], v[26:33], v[226:233], 0, v193, v193 op_sel_hi:[0,0,0]
	v_mfma_scale_f32_16x16x128_f8f6f4 v[126:129], v[18:25], v[234:241], 0, v193, v193 op_sel_hi:[0,0,0]
	v_mfma_scale_f32_16x16x128_f8f6f4 v[122:125], v[26:33], v[234:241], 0, v193, v193 op_sel_hi:[0,0,0]
	v_mfma_scale_f32_16x16x128_f8f6f4 v[110:113], v[18:25], v[242:249], 0, v193, v193 op_sel_hi:[0,0,0]
	v_mfma_scale_f32_16x16x128_f8f6f4 v[106:109], v[26:33], v[242:249], 0, v193, v193 op_sel_hi:[0,0,0]
	s_setprio 0
	s_setprio 1
	v_mfma_scale_f32_16x16x128_f8f6f4 v[150:153], v[2:9], v[218:225], 0, v193, v193 op_sel_hi:[0,0,0]
	v_mfma_scale_f32_16x16x128_f8f6f4 v[146:149], v[10:17], v[218:225], 0, v193, v193 op_sel_hi:[0,0,0]
	v_mfma_scale_f32_16x16x128_f8f6f4 v[134:137], v[2:9], v[226:233], 0, v193, v193 op_sel_hi:[0,0,0]
	v_mfma_scale_f32_16x16x128_f8f6f4 v[130:133], v[10:17], v[226:233], 0, v193, v193 op_sel_hi:[0,0,0]
	v_mfma_scale_f32_16x16x128_f8f6f4 v[118:121], v[2:9], v[234:241], 0, v193, v193 op_sel_hi:[0,0,0]
	v_mfma_scale_f32_16x16x128_f8f6f4 v[114:117], v[10:17], v[234:241], 0, v193, v193 op_sel_hi:[0,0,0]
	v_mfma_scale_f32_16x16x128_f8f6f4 v[102:105], v[2:9], v[242:249], 0, v193, v193 op_sel_hi:[0,0,0]
	v_mfma_scale_f32_16x16x128_f8f6f4 v[98:101], v[10:17], v[242:249], 0, v193, v193 op_sel_hi:[0,0,0]
	s_setprio 0
	s_barrier
	s_mov_b32 m0, s27
	v_lshl_add_u64 v[184:185], v[182:183], 0, v[162:163]
	ds_read_b128 v[218:221], v175 offset:16384
	ds_read_b128 v[222:225], v175 offset:17408
	ds_read_b128 v[226:229], v175 offset:18432
	ds_read_b128 v[230:233], v175 offset:19456
	ds_read_b128 v[234:237], v175 offset:20480
	ds_read_b128 v[238:241], v175 offset:21504
	ds_read_b128 v[242:245], v175 offset:22528
	ds_read_b128 v[246:249], v175 offset:23552
	global_load_lds_dwordx4 v[184:185], off
	v_lshl_add_u64 v[186:187], v[182:183], 0, v[164:165]
	s_mov_b32 m0, s33
	v_lshl_add_u64 v[204:205], v[182:183], 0, s[36:37]
	global_load_lds_dwordx4 v[186:187], off
	v_lshl_add_u64 v[206:207], v[204:205], 0, v[162:163]
	s_mov_b32 m0, s48
	v_lshl_add_u64 v[204:205], v[204:205], 0, v[164:165]
	global_load_lds_dwordx4 v[206:207], off
	s_mov_b32 m0, s49
	s_add_u32 vcc_lo, s12, s18
	global_load_lds_dwordx4 v[204:205], off
	s_addc_u32 vcc_hi, s13, 0
	s_mov_b32 m0, s50
	v_mov_b32_e32 v191, v0
	global_load_lds_dwordx4 v190, vcc
	s_mov_b32 m0, s51
	v_mov_b32_e32 v189, v0
	global_load_lds_dwordx4 v188, vcc
	s_waitcnt vmcnt(8)
	s_waitcnt lgkmcnt(0)
	v_lshl_add_u64 v[190:191], vcc, 0, v[190:191]
	v_lshl_add_u64 v[188:189], vcc, 0, v[188:189]
	s_barrier
	s_setprio 1
	s_waitcnt lgkmcnt(0)
	v_mfma_scale_f32_16x16x128_f8f6f4 v[94:97], v[18:25], v[218:225], 0, v193, v193 op_sel_hi:[0,0,0]
	v_mfma_scale_f32_16x16x128_f8f6f4 v[90:93], v[26:33], v[218:225], 0, v193, v193 op_sel_hi:[0,0,0]
	v_mfma_scale_f32_16x16x128_f8f6f4 v[78:81], v[18:25], v[226:233], 0, v193, v193 op_sel_hi:[0,0,0]
	v_mfma_scale_f32_16x16x128_f8f6f4 v[74:77], v[26:33], v[226:233], 0, v193, v193 op_sel_hi:[0,0,0]
	v_mfma_scale_f32_16x16x128_f8f6f4 v[50:53], v[18:25], v[234:241], 0, v193, v193 op_sel_hi:[0,0,0]
	v_mfma_scale_f32_16x16x128_f8f6f4 v[42:45], v[26:33], v[234:241], 0, v193, v193 op_sel_hi:[0,0,0]
	v_mfma_scale_f32_16x16x128_f8f6f4 v[38:41], v[18:25], v[242:249], 0, v193, v193 op_sel_hi:[0,0,0]
	v_mfma_scale_f32_16x16x128_f8f6f4 v[34:37], v[26:33], v[242:249], 0, v193, v193 op_sel_hi:[0,0,0]
	s_setprio 0
	s_setprio 1
	v_mfma_scale_f32_16x16x128_f8f6f4 v[86:89], v[2:9], v[218:225], 0, v193, v193 op_sel_hi:[0,0,0]
	v_mfma_scale_f32_16x16x128_f8f6f4 v[82:85], v[10:17], v[218:225], 0, v193, v193 op_sel_hi:[0,0,0]
	v_mfma_scale_f32_16x16x128_f8f6f4 v[62:65], v[2:9], v[226:233], 0, v193, v193 op_sel_hi:[0,0,0]
	v_mfma_scale_f32_16x16x128_f8f6f4 v[58:61], v[10:17], v[226:233], 0, v193, v193 op_sel_hi:[0,0,0]
	v_mfma_scale_f32_16x16x128_f8f6f4 v[66:69], v[2:9], v[234:241], 0, v193, v193 op_sel_hi:[0,0,0]
	v_mfma_scale_f32_16x16x128_f8f6f4 v[70:73], v[10:17], v[234:241], 0, v193, v193 op_sel_hi:[0,0,0]
	v_mfma_scale_f32_16x16x128_f8f6f4 v[46:49], v[2:9], v[242:249], 0, v193, v193 op_sel_hi:[0,0,0]
	v_mfma_scale_f32_16x16x128_f8f6f4 v[54:57], v[10:17], v[242:249], 0, v193, v193 op_sel_hi:[0,0,0]
	s_setprio 0
	s_barrier
	v_add_u32_e32 v14, s56, v197
	v_add_u32_e32 v30, s69, v197
	ds_read_b128 v[2:5], v14
	ds_read_b128 v[6:9], v14 offset:1024
	ds_read_b128 v[10:13], v14 offset:2048
	ds_read_b128 v[14:17], v14 offset:3072
	ds_read_b128 v[18:21], v30
	ds_read_b128 v[22:25], v30 offset:1024
	ds_read_b128 v[26:29], v30 offset:2048
	ds_read_b128 v[30:33], v30 offset:3072
	s_mov_b32 m0, s52
	ds_read_b128 v[218:221], v175 offset:32768
	ds_read_b128 v[222:225], v175 offset:33792
	ds_read_b128 v[226:229], v175 offset:34816
	ds_read_b128 v[230:233], v175 offset:35840
	ds_read_b128 v[234:237], v175 offset:36864
	ds_read_b128 v[238:241], v175 offset:37888
	ds_read_b128 v[242:245], v175 offset:38912
	ds_read_b128 v[246:249], v175 offset:39936
	global_load_lds_dwordx4 v171, vcc
	s_mov_b32 m0, s54
	s_nop 0
	global_load_lds_dwordx4 v169, vcc
	s_waitcnt vmcnt(8)
	s_waitcnt lgkmcnt(0)
	s_barrier
	s_setprio 1
	s_waitcnt lgkmcnt(0)
	v_mfma_scale_f32_16x16x128_f8f6f4 v[158:161], v[2:9], v[218:225], v[158:161], v193, v193 op_sel_hi:[0,0,0]
	v_mfma_scale_f32_16x16x128_f8f6f4 v[154:157], v[10:17], v[218:225], v[154:157], v193, v193 op_sel_hi:[0,0,0]
	v_mfma_scale_f32_16x16x128_f8f6f4 v[142:145], v[2:9], v[226:233], v[142:145], v193, v193 op_sel_hi:[0,0,0]
	v_mfma_scale_f32_16x16x128_f8f6f4 v[138:141], v[10:17], v[226:233], v[138:141], v193, v193 op_sel_hi:[0,0,0]
	v_mfma_scale_f32_16x16x128_f8f6f4 v[126:129], v[2:9], v[234:241], v[126:129], v193, v193 op_sel_hi:[0,0,0]
	v_mfma_scale_f32_16x16x128_f8f6f4 v[122:125], v[10:17], v[234:241], v[122:125], v193, v193 op_sel_hi:[0,0,0]
	v_mfma_scale_f32_16x16x128_f8f6f4 v[110:113], v[2:9], v[242:249], v[110:113], v193, v193 op_sel_hi:[0,0,0]
	v_mfma_scale_f32_16x16x128_f8f6f4 v[106:109], v[10:17], v[242:249], v[106:109], v193, v193 op_sel_hi:[0,0,0]
	s_setprio 0
	s_setprio 1
	v_mfma_scale_f32_16x16x128_f8f6f4 v[150:153], v[18:25], v[218:225], v[150:153], v193, v193 op_sel_hi:[0,0,0]
	v_mfma_scale_f32_16x16x128_f8f6f4 v[146:149], v[26:33], v[218:225], v[146:149], v193, v193 op_sel_hi:[0,0,0]
	v_mfma_scale_f32_16x16x128_f8f6f4 v[134:137], v[18:25], v[226:233], v[134:137], v193, v193 op_sel_hi:[0,0,0]
	v_mfma_scale_f32_16x16x128_f8f6f4 v[130:133], v[26:33], v[226:233], v[130:133], v193, v193 op_sel_hi:[0,0,0]
	v_mfma_scale_f32_16x16x128_f8f6f4 v[118:121], v[18:25], v[234:241], v[118:121], v193, v193 op_sel_hi:[0,0,0]
	v_mfma_scale_f32_16x16x128_f8f6f4 v[114:117], v[26:33], v[234:241], v[114:117], v193, v193 op_sel_hi:[0,0,0]
	v_mfma_scale_f32_16x16x128_f8f6f4 v[102:105], v[18:25], v[242:249], v[102:105], v193, v193 op_sel_hi:[0,0,0]
	v_mfma_scale_f32_16x16x128_f8f6f4 v[98:101], v[26:33], v[242:249], v[98:101], v193, v193 op_sel_hi:[0,0,0]
	s_setprio 0
	s_barrier
	s_mov_b32 m0, s61
	v_lshl_add_u64 v[184:185], v[184:185], 0, s[38:39]
	ds_read_b128 v[218:221], v175 offset:49152
	ds_read_b128 v[222:225], v175 offset:50176
	ds_read_b128 v[226:229], v175 offset:51200
	ds_read_b128 v[230:233], v175 offset:52224
	ds_read_b128 v[234:237], v175 offset:53248
	ds_read_b128 v[238:241], v175 offset:54272
	ds_read_b128 v[242:245], v175 offset:55296
	ds_read_b128 v[246:249], v175 offset:56320
	global_load_lds_dwordx4 v[184:185], off
	v_lshl_add_u64 v[184:185], v[186:187], 0, s[38:39]
	s_mov_b32 m0, s64
	v_lshl_add_u64 v[182:183], v[182:183], 0, s[40:41]
	global_load_lds_dwordx4 v[184:185], off
	v_lshl_add_u64 v[184:185], v[182:183], 0, v[162:163]
	s_mov_b32 m0, s70
	v_lshl_add_u64 v[182:183], v[182:183], 0, v[164:165]
	global_load_lds_dwordx4 v[184:185], off
	s_mov_b32 m0, s71
	s_nop 0
	global_load_lds_dwordx4 v[182:183], off
	v_lshl_add_u64 v[182:183], v[190:191], 0, s[38:39]
	s_mov_b32 m0, s67
	s_nop 0
	global_load_lds_dwordx4 v[182:183], off
	v_lshl_add_u64 v[182:183], v[188:189], 0, s[38:39]
	s_mov_b32 m0, s68
	s_nop 0
	global_load_lds_dwordx4 v[182:183], off
	s_waitcnt vmcnt(8)
	s_waitcnt lgkmcnt(0)
	s_barrier
	s_setprio 1
	s_waitcnt lgkmcnt(0)
	v_mfma_scale_f32_16x16x128_f8f6f4 v[94:97], v[2:9], v[218:225], v[94:97], v193, v193 op_sel_hi:[0,0,0]
	v_mfma_scale_f32_16x16x128_f8f6f4 v[90:93], v[10:17], v[218:225], v[90:93], v193, v193 op_sel_hi:[0,0,0]
	v_mfma_scale_f32_16x16x128_f8f6f4 v[78:81], v[2:9], v[226:233], v[78:81], v193, v193 op_sel_hi:[0,0,0]
	v_mfma_scale_f32_16x16x128_f8f6f4 v[74:77], v[10:17], v[226:233], v[74:77], v193, v193 op_sel_hi:[0,0,0]
	v_mfma_scale_f32_16x16x128_f8f6f4 v[50:53], v[2:9], v[234:241], v[50:53], v193, v193 op_sel_hi:[0,0,0]
	v_mfma_scale_f32_16x16x128_f8f6f4 v[42:45], v[10:17], v[234:241], v[42:45], v193, v193 op_sel_hi:[0,0,0]
	v_mfma_scale_f32_16x16x128_f8f6f4 v[38:41], v[2:9], v[242:249], v[38:41], v193, v193 op_sel_hi:[0,0,0]
	v_mfma_scale_f32_16x16x128_f8f6f4 v[34:37], v[10:17], v[242:249], v[34:37], v193, v193 op_sel_hi:[0,0,0]
	s_setprio 0
	s_setprio 1
	v_mfma_scale_f32_16x16x128_f8f6f4 v[86:89], v[18:25], v[218:225], v[86:89], v193, v193 op_sel_hi:[0,0,0]
	v_mfma_scale_f32_16x16x128_f8f6f4 v[82:85], v[26:33], v[218:225], v[82:85], v193, v193 op_sel_hi:[0,0,0]
	v_mfma_scale_f32_16x16x128_f8f6f4 v[62:65], v[18:25], v[226:233], v[62:65], v193, v193 op_sel_hi:[0,0,0]
	v_mfma_scale_f32_16x16x128_f8f6f4 v[58:61], v[26:33], v[226:233], v[58:61], v193, v193 op_sel_hi:[0,0,0]
	v_mfma_scale_f32_16x16x128_f8f6f4 v[66:69], v[18:25], v[234:241], v[66:69], v193, v193 op_sel_hi:[0,0,0]
	v_mfma_scale_f32_16x16x128_f8f6f4 v[70:73], v[26:33], v[234:241], v[70:73], v193, v193 op_sel_hi:[0,0,0]
	v_mfma_scale_f32_16x16x128_f8f6f4 v[46:49], v[18:25], v[242:249], v[46:49], v193, v193 op_sel_hi:[0,0,0]
	v_mfma_scale_f32_16x16x128_f8f6f4 v[54:57], v[26:33], v[242:249], v[54:57], v193, v193 op_sel_hi:[0,0,0]
	s_setprio 0
	s_barrier
	s_cmp_eq_u32 s96, 0
	s_cselect_b64 s[18:19], -1, 0
	s_and_b64 s[18:19], s[18:19], s[88:89]
	s_xor_b64 s[62:63], s[18:19], -1
	s_and_b64 s[62:63], s[62:63], s[88:89]
	s_andn2_b64 s[92:93], s[92:93], exec
	s_and_b64 s[62:63], s[62:63], exec
	s_and_b64 s[18:19], s[18:19], s[0:1]
	s_or_b64 s[92:93], s[92:93], s[62:63]
	s_and_saveexec_b64 s[96:97], s[18:19]
	s_cbranch_execz .Lpe1_LBB0_1058
	s_mov_b64 s[18:19], exec
	v_mbcnt_lo_u32_b32 v2, s18, 0
	v_mbcnt_hi_u32_b32 v2, s19, v2
	v_cmp_eq_u32_e32 vcc, 0, v2
	s_and_saveexec_b64 s[88:89], vcc
	s_cbranch_execz .Lpe1_LBB0_1057
	s_bcnt1_i32_b64 s18, s[18:19]
	v_mov_b32_e32 v2, s18
	global_atomic_add v0, v2, s[90:91]
	s_branch .Lpe1_LBB0_1057

.Lpe1_Le1_tok_done:
	s_andn2_b64 s[18:19], s[88:89], exec
	s_and_b64 s[62:63], s[92:93], exec
	s_add_i32 s23, s23, 2
	s_or_b64 s[88:89], s[18:19], s[62:63]
	s_cmp_gt_u32 s23, 5
	s_branch .LBB0_1059

.LBB0_1109:
	s_lshl_b32 s4, s3, 4
	s_ashr_i32 s5, s4, 31
	s_lshl_b64 s[4:5], s[4:5], 2
	s_add_u32 s8, s65, s4
	s_waitcnt vmcnt(0)
	v_mov_b32_e32 v183, v0
	v_mov_b32_e32 v187, v0
	s_addc_u32 s9, s66, s5
	s_mov_b32 s12, 0
	s_cmp_eq_u32 s12, 4
	s_cselect_b64 s[4:5], -1, 0
	s_and_b64 s[10:11], s[6:7], s[4:5]
	s_lshl_b32 s24, s12, 7
	v_lshl_add_u64 v[2:3], v[190:191], 0, s[24:25]
	v_lshl_add_u64 v[2:3], v[2:3], 0, s[42:43]
	v_cndmask_b32_e64 v192, v2, v180, s[4:5]
	v_add_u32_e32 v2, s18, v189
	v_add_u32_e32 v14, s27, v189
	v_cndmask_b32_e64 v193, v3, v181, s[4:5]
	ds_read_b128 v[18:21], v2
	ds_read_b128 v[22:25], v2 offset:1024
	ds_read_b128 v[26:29], v2 offset:2048
	ds_read_b128 v[30:33], v2 offset:3072
	ds_read_b128 v[2:5], v14
	ds_read_b128 v[6:9], v14 offset:1024
	ds_read_b128 v[10:13], v14 offset:2048
	ds_read_b128 v[14:17], v14 offset:3072
	s_add_i32 s13, s24, 0x100
	s_and_b64 s[10:11], s[4:5], exec
	v_cndmask_b32_e64 v196, v184, v172, s[4:5]
	v_cndmask_b32_e64 v194, v188, v174, s[4:5]
	v_cndmask_b32_e64 v175, v182, v176, s[4:5]
	v_cndmask_b32_e64 v173, v186, v178, s[4:5]
	s_cselect_b32 s10, 0, s13
	s_add_u32 s4, s84, s24
	s_addc_u32 s5, s85, 0
	v_lshl_add_u64 v[206:207], s[4:5], 0, v[182:183]
	v_lshl_add_u64 v[206:207], v[206:207], 0, s[38:39]
	s_add_i32 m0, s48, 0xc000
	ds_read_b128 v[224:227], v217
	ds_read_b128 v[228:231], v217 offset:1024
	ds_read_b128 v[232:235], v217 offset:2048
	ds_read_b128 v[236:239], v217 offset:3072
	ds_read_b128 v[240:243], v217 offset:4096
	ds_read_b128 v[244:247], v217 offset:5120
	ds_read_b128 v[198:201], v217 offset:6144
	ds_read_b128 v[202:205], v217 offset:7168
	global_load_lds_dwordx4 v[206:207], off
	v_lshl_add_u64 v[206:207], s[4:5], 0, v[186:187]
	v_lshl_add_u64 v[206:207], v[206:207], 0, s[38:39]
	s_add_i32 m0, s48, 0xe000
	s_nop 0
	global_load_lds_dwordx4 v[206:207], off
	s_waitcnt vmcnt(8)
	s_waitcnt lgkmcnt(0)
	s_barrier
	s_setprio 1
	s_waitcnt lgkmcnt(0)
	v_mfma_scale_f32_16x16x128_f8f6f4 v[158:161], v[18:25], v[224:231], 0, v1, v1 op_sel_hi:[0,0,0]
	v_mfma_scale_f32_16x16x128_f8f6f4 v[154:157], v[26:33], v[224:231], 0, v1, v1 op_sel_hi:[0,0,0]
	v_mfma_scale_f32_16x16x128_f8f6f4 v[142:145], v[18:25], v[232:239], 0, v1, v1 op_sel_hi:[0,0,0]
	v_mfma_scale_f32_16x16x128_f8f6f4 v[138:141], v[26:33], v[232:239], 0, v1, v1 op_sel_hi:[0,0,0]
	v_mfma_scale_f32_16x16x128_f8f6f4 v[126:129], v[18:25], v[240:247], 0, v1, v1 op_sel_hi:[0,0,0]
	v_mfma_scale_f32_16x16x128_f8f6f4 v[122:125], v[26:33], v[240:247], 0, v1, v1 op_sel_hi:[0,0,0]
	v_mfma_scale_f32_16x16x128_f8f6f4 v[110:113], v[18:25], v[198:205], 0, v1, v1 op_sel_hi:[0,0,0]
	v_mfma_scale_f32_16x16x128_f8f6f4 v[106:109], v[26:33], v[198:205], 0, v1, v1 op_sel_hi:[0,0,0]
	s_setprio 0
	s_setprio 1
	v_mfma_scale_f32_16x16x128_f8f6f4 v[150:153], v[2:9], v[224:231], 0, v1, v1 op_sel_hi:[0,0,0]
	v_mfma_scale_f32_16x16x128_f8f6f4 v[146:149], v[10:17], v[224:231], 0, v1, v1 op_sel_hi:[0,0,0]
	v_mfma_scale_f32_16x16x128_f8f6f4 v[134:137], v[2:9], v[232:239], 0, v1, v1 op_sel_hi:[0,0,0]
	v_mfma_scale_f32_16x16x128_f8f6f4 v[130:133], v[10:17], v[232:239], 0, v1, v1 op_sel_hi:[0,0,0]
	v_mfma_scale_f32_16x16x128_f8f6f4 v[118:121], v[2:9], v[240:247], 0, v1, v1 op_sel_hi:[0,0,0]
	v_mfma_scale_f32_16x16x128_f8f6f4 v[114:117], v[10:17], v[240:247], 0, v1, v1 op_sel_hi:[0,0,0]
	v_mfma_scale_f32_16x16x128_f8f6f4 v[102:105], v[2:9], v[198:205], 0, v1, v1 op_sel_hi:[0,0,0]
	v_mfma_scale_f32_16x16x128_f8f6f4 v[98:101], v[10:17], v[198:205], 0, v1, v1 op_sel_hi:[0,0,0]
	s_setprio 0
	s_barrier
	s_mov_b32 m0, s19
	v_lshl_add_u64 v[198:199], v[192:193], 0, v[166:167]
	ds_read_b128 v[224:227], v217 offset:16384
	ds_read_b128 v[228:231], v217 offset:17408
	ds_read_b128 v[232:235], v217 offset:18432
	ds_read_b128 v[236:239], v217 offset:19456
	ds_read_b128 v[240:243], v217 offset:20480
	ds_read_b128 v[244:247], v217 offset:21504
	ds_read_b128 v[202:205], v217 offset:22528
	ds_read_b128 v[206:209], v217 offset:23552
	global_load_lds_dwordx4 v[198:199], off
	v_lshl_add_u64 v[200:201], v[192:193], 0, v[168:169]
	s_mov_b32 m0, s26
	v_lshl_add_u64 v[214:215], v[192:193], 0, s[74:75]
	global_load_lds_dwordx4 v[200:201], off
	v_lshl_add_u64 v[248:249], v[214:215], 0, v[166:167]
	s_mov_b32 m0, s33
	v_lshl_add_u64 v[214:215], v[214:215], 0, v[168:169]
	global_load_lds_dwordx4 v[248:249], off
	s_mov_b32 m0, s45
	s_add_u32 s4, s84, s10
	global_load_lds_dwordx4 v[214:215], off
	s_addc_u32 s5, s85, 0
	s_mov_b32 m0, s48
	v_mov_b32_e32 v197, v0
	global_load_lds_dwordx4 v196, s[4:5]
	s_mov_b32 m0, s49
	v_mov_b32_e32 v195, v0
	global_load_lds_dwordx4 v194, s[4:5]
	s_waitcnt vmcnt(8)
	s_waitcnt lgkmcnt(0)
	v_lshl_add_u64 v[196:197], s[4:5], 0, v[196:197]
	v_lshl_add_u64 v[194:195], s[4:5], 0, v[194:195]
	s_barrier
	s_setprio 1
	s_waitcnt lgkmcnt(0)
	v_mfma_scale_f32_16x16x128_f8f6f4 v[94:97], v[18:25], v[224:231], 0, v1, v1 op_sel_hi:[0,0,0]
	v_mfma_scale_f32_16x16x128_f8f6f4 v[90:93], v[26:33], v[224:231], 0, v1, v1 op_sel_hi:[0,0,0]
	v_mfma_scale_f32_16x16x128_f8f6f4 v[78:81], v[18:25], v[232:239], 0, v1, v1 op_sel_hi:[0,0,0]
	v_mfma_scale_f32_16x16x128_f8f6f4 v[74:77], v[26:33], v[232:239], 0, v1, v1 op_sel_hi:[0,0,0]
	v_mfma_scale_f32_16x16x128_f8f6f4 v[54:57], v[18:25], v[240:247], 0, v1, v1 op_sel_hi:[0,0,0]
	v_mfma_scale_f32_16x16x128_f8f6f4 v[50:53], v[26:33], v[240:247], 0, v1, v1 op_sel_hi:[0,0,0]
	v_mfma_scale_f32_16x16x128_f8f6f4 v[38:41], v[18:25], v[202:209], 0, v1, v1 op_sel_hi:[0,0,0]
	v_mfma_scale_f32_16x16x128_f8f6f4 v[34:37], v[26:33], v[202:209], 0, v1, v1 op_sel_hi:[0,0,0]
	s_setprio 0
	s_setprio 1
	v_mfma_scale_f32_16x16x128_f8f6f4 v[86:89], v[2:9], v[224:231], 0, v1, v1 op_sel_hi:[0,0,0]
	v_mfma_scale_f32_16x16x128_f8f6f4 v[82:85], v[10:17], v[224:231], 0, v1, v1 op_sel_hi:[0,0,0]
	v_mfma_scale_f32_16x16x128_f8f6f4 v[70:73], v[2:9], v[232:239], 0, v1, v1 op_sel_hi:[0,0,0]
	v_mfma_scale_f32_16x16x128_f8f6f4 v[58:61], v[10:17], v[232:239], 0, v1, v1 op_sel_hi:[0,0,0]
	v_mfma_scale_f32_16x16x128_f8f6f4 v[66:69], v[2:9], v[240:247], 0, v1, v1 op_sel_hi:[0,0,0]
	v_mfma_scale_f32_16x16x128_f8f6f4 v[62:65], v[10:17], v[240:247], 0, v1, v1 op_sel_hi:[0,0,0]
	v_mfma_scale_f32_16x16x128_f8f6f4 v[46:49], v[2:9], v[202:209], 0, v1, v1 op_sel_hi:[0,0,0]
	v_mfma_scale_f32_16x16x128_f8f6f4 v[42:45], v[10:17], v[202:209], 0, v1, v1 op_sel_hi:[0,0,0]
	s_setprio 0
	s_barrier
	v_add_u32_e32 v14, s52, v189
	v_add_u32_e32 v30, s67, v189
	ds_read_b128 v[2:5], v14
	ds_read_b128 v[6:9], v14 offset:1024
	ds_read_b128 v[10:13], v14 offset:2048
	ds_read_b128 v[14:17], v14 offset:3072
	ds_read_b128 v[18:21], v30
	ds_read_b128 v[22:25], v30 offset:1024
	ds_read_b128 v[26:29], v30 offset:2048
	ds_read_b128 v[30:33], v30 offset:3072
	s_mov_b32 m0, s50
	ds_read_b128 v[202:205], v217 offset:32768
	ds_read_b128 v[206:209], v217 offset:33792
	ds_read_b128 v[224:227], v217 offset:34816
	ds_read_b128 v[228:231], v217 offset:35840
	ds_read_b128 v[232:235], v217 offset:36864
	ds_read_b128 v[236:239], v217 offset:37888
	ds_read_b128 v[240:243], v217 offset:38912
	ds_read_b128 v[244:247], v217 offset:39936
	global_load_lds_dwordx4 v175, s[4:5]
	s_mov_b32 m0, s51
	s_nop 0
	global_load_lds_dwordx4 v173, s[4:5]
	s_waitcnt vmcnt(8)
	s_waitcnt lgkmcnt(0)
	s_barrier
	s_setprio 1
	s_waitcnt lgkmcnt(0)
	v_mfma_scale_f32_16x16x128_f8f6f4 v[158:161], v[2:9], v[202:209], v[158:161], v1, v1 op_sel_hi:[0,0,0]
	v_mfma_scale_f32_16x16x128_f8f6f4 v[154:157], v[10:17], v[202:209], v[154:157], v1, v1 op_sel_hi:[0,0,0]
	v_mfma_scale_f32_16x16x128_f8f6f4 v[142:145], v[2:9], v[224:231], v[142:145], v1, v1 op_sel_hi:[0,0,0]
	v_mfma_scale_f32_16x16x128_f8f6f4 v[138:141], v[10:17], v[224:231], v[138:141], v1, v1 op_sel_hi:[0,0,0]
	v_mfma_scale_f32_16x16x128_f8f6f4 v[126:129], v[2:9], v[232:239], v[126:129], v1, v1 op_sel_hi:[0,0,0]
	v_mfma_scale_f32_16x16x128_f8f6f4 v[122:125], v[10:17], v[232:239], v[122:125], v1, v1 op_sel_hi:[0,0,0]
	v_mfma_scale_f32_16x16x128_f8f6f4 v[110:113], v[2:9], v[240:247], v[110:113], v1, v1 op_sel_hi:[0,0,0]
	v_mfma_scale_f32_16x16x128_f8f6f4 v[106:109], v[10:17], v[240:247], v[106:109], v1, v1 op_sel_hi:[0,0,0]
	s_setprio 0
	s_setprio 1
	v_mfma_scale_f32_16x16x128_f8f6f4 v[150:153], v[18:25], v[202:209], v[150:153], v1, v1 op_sel_hi:[0,0,0]
	v_mfma_scale_f32_16x16x128_f8f6f4 v[146:149], v[26:33], v[202:209], v[146:149], v1, v1 op_sel_hi:[0,0,0]
	v_mfma_scale_f32_16x16x128_f8f6f4 v[134:137], v[18:25], v[224:231], v[134:137], v1, v1 op_sel_hi:[0,0,0]
	v_mfma_scale_f32_16x16x128_f8f6f4 v[130:133], v[26:33], v[224:231], v[130:133], v1, v1 op_sel_hi:[0,0,0]
	v_mfma_scale_f32_16x16x128_f8f6f4 v[118:121], v[18:25], v[232:239], v[118:121], v1, v1 op_sel_hi:[0,0,0]
	v_mfma_scale_f32_16x16x128_f8f6f4 v[114:117], v[26:33], v[232:239], v[114:117], v1, v1 op_sel_hi:[0,0,0]
	v_mfma_scale_f32_16x16x128_f8f6f4 v[102:105], v[18:25], v[240:247], v[102:105], v1, v1 op_sel_hi:[0,0,0]
	v_mfma_scale_f32_16x16x128_f8f6f4 v[98:101], v[26:33], v[240:247], v[98:101], v1, v1 op_sel_hi:[0,0,0]
	s_setprio 0
	s_barrier
	s_mov_b32 m0, s54
	v_lshl_add_u64 v[198:199], v[198:199], 0, s[38:39]
	ds_read_b128 v[202:205], v217 offset:49152
	ds_read_b128 v[206:209], v217 offset:50176
	ds_read_b128 v[224:227], v217 offset:51200
	ds_read_b128 v[228:231], v217 offset:52224
	ds_read_b128 v[232:235], v217 offset:53248
	ds_read_b128 v[236:239], v217 offset:54272
	ds_read_b128 v[240:243], v217 offset:55296
	ds_read_b128 v[244:247], v217 offset:56320
	global_load_lds_dwordx4 v[198:199], off
	v_lshl_add_u64 v[198:199], v[200:201], 0, s[38:39]
	s_mov_b32 m0, s56
	v_lshl_add_u64 v[192:193], v[192:193], 0, s[76:77]
	global_load_lds_dwordx4 v[198:199], off
	v_lshl_add_u64 v[198:199], v[192:193], 0, v[166:167]
	s_mov_b32 m0, s68
	v_lshl_add_u64 v[192:193], v[192:193], 0, v[168:169]
	global_load_lds_dwordx4 v[198:199], off
	s_mov_b32 m0, s69
	s_nop 0
	global_load_lds_dwordx4 v[192:193], off
	v_lshl_add_u64 v[192:193], v[196:197], 0, s[38:39]
	s_mov_b32 m0, s61
	s_nop 0
	global_load_lds_dwordx4 v[192:193], off
	v_lshl_add_u64 v[192:193], v[194:195], 0, s[38:39]
	s_mov_b32 m0, s64
	s_nop 0
	global_load_lds_dwordx4 v[192:193], off
	s_waitcnt vmcnt(8)
	s_waitcnt lgkmcnt(0)
	s_barrier
	s_setprio 1
	s_waitcnt lgkmcnt(0)
	v_mfma_scale_f32_16x16x128_f8f6f4 v[94:97], v[2:9], v[202:209], v[94:97], v1, v1 op_sel_hi:[0,0,0]
	v_mfma_scale_f32_16x16x128_f8f6f4 v[90:93], v[10:17], v[202:209], v[90:93], v1, v1 op_sel_hi:[0,0,0]
	v_mfma_scale_f32_16x16x128_f8f6f4 v[78:81], v[2:9], v[224:231], v[78:81], v1, v1 op_sel_hi:[0,0,0]
	v_mfma_scale_f32_16x16x128_f8f6f4 v[74:77], v[10:17], v[224:231], v[74:77], v1, v1 op_sel_hi:[0,0,0]
	v_mfma_scale_f32_16x16x128_f8f6f4 v[54:57], v[2:9], v[232:239], v[54:57], v1, v1 op_sel_hi:[0,0,0]
	v_mfma_scale_f32_16x16x128_f8f6f4 v[50:53], v[10:17], v[232:239], v[50:53], v1, v1 op_sel_hi:[0,0,0]
	v_mfma_scale_f32_16x16x128_f8f6f4 v[38:41], v[2:9], v[240:247], v[38:41], v1, v1 op_sel_hi:[0,0,0]
	v_mfma_scale_f32_16x16x128_f8f6f4 v[34:37], v[10:17], v[240:247], v[34:37], v1, v1 op_sel_hi:[0,0,0]
	s_setprio 0
	s_setprio 1
	v_mfma_scale_f32_16x16x128_f8f6f4 v[86:89], v[18:25], v[202:209], v[86:89], v1, v1 op_sel_hi:[0,0,0]
	v_mfma_scale_f32_16x16x128_f8f6f4 v[82:85], v[26:33], v[202:209], v[82:85], v1, v1 op_sel_hi:[0,0,0]
	v_mfma_scale_f32_16x16x128_f8f6f4 v[70:73], v[18:25], v[224:231], v[70:73], v1, v1 op_sel_hi:[0,0,0]
	v_mfma_scale_f32_16x16x128_f8f6f4 v[58:61], v[26:33], v[224:231], v[58:61], v1, v1 op_sel_hi:[0,0,0]
	v_mfma_scale_f32_16x16x128_f8f6f4 v[66:69], v[18:25], v[232:239], v[66:69], v1, v1 op_sel_hi:[0,0,0]
	v_mfma_scale_f32_16x16x128_f8f6f4 v[62:65], v[26:33], v[232:239], v[62:65], v1, v1 op_sel_hi:[0,0,0]
	v_mfma_scale_f32_16x16x128_f8f6f4 v[46:49], v[18:25], v[240:247], v[46:49], v1, v1 op_sel_hi:[0,0,0]
	v_mfma_scale_f32_16x16x128_f8f6f4 v[42:45], v[26:33], v[240:247], v[42:45], v1, v1 op_sel_hi:[0,0,0]
	s_setprio 0
	s_barrier
	s_add_i32 s4, s12, 2
	s_cmp_gt_u32 s12, 3
	s_mov_b32 s12, s4
	s_branch .LBB0_1112
